# v4b + P8 conv: rmsnorm gain kept in registers; vmcnt waits of both conv copies re-derived
# speedup vs baseline: 1.0220x; 1.0066x over previous
.LBB0_981:
	v_readlane_b32 s4, v252, 0
	s_cmp_lt_i32 s4, 9
	s_cselect_b64 s[0:1], -1, 0
	s_and_b64 s[0:1], s[0:1], s[2:3]
	v_readlane_b32 s5, v252, 1
	v_readlane_b32 s6, v252, 2
	v_readlane_b32 s7, v252, 3
	v_writelane_b32 v252, s0, 29
	s_andn2_b64 vcc, exec, s[0:1]
	s_nop 0
	v_writelane_b32 v252, s1, 30
	s_cbranch_vccnz .LBB0_1004
	v_readlane_b32 s0, v252, 4
	v_readlane_b32 s1, v252, 5
	s_cmpk_gt_i32 s90, 0xff
	s_cbranch_scc1 .LBB0_1004
	v_mbcnt_lo_u32_b32 v4, -1, 0
	v_mbcnt_hi_u32_b32 v4, -1, v4
	v_and_b32_e32 v6, 64, v4
	v_xor_b32_e32 v5, 1, v4
	v_add_u32_e32 v6, 64, v6
	v_cmp_lt_i32_e32 vcc, v5, v6
	s_load_dwordx2 s[2:3], s[0:1], 0xf0
	s_load_dwordx2 s[4:5], s[0:1], 0x90
	s_load_dwordx2 s[6:7], s[0:1], 0xa0
	v_cndmask_b32_e32 v5, v4, v5, vcc
	s_waitcnt vmcnt(0)
	v_lshlrev_b32_e32 v62, 2, v5
	v_xor_b32_e32 v5, 2, v4
	s_and_b32 s0, s90, 8
	v_cmp_lt_i32_e32 vcc, v5, v6
	s_cmp_eq_u32 s0, 0
	v_and_b32_e32 v3, 7, v0
	v_cndmask_b32_e32 v5, v4, v5, vcc
	s_cselect_b64 s[96:97], -1, 0
	s_cmp_lg_u32 s0, 0
	v_lshlrev_b32_e32 v63, 2, v5
	v_xor_b32_e32 v5, 4, v4
	s_mov_b32 s14, s90
	s_cselect_b64 s[90:91], -1, 0
	s_waitcnt lgkmcnt(0)
	s_add_u32 s0, s2, 0x68200000
	v_lshlrev_b32_e32 v36, 4, v3
	v_mov_b32_e32 v37, 0
	v_cmp_lt_i32_e32 vcc, v5, v6
	s_addc_u32 s1, s3, 0
	v_lshl_add_u64 v[6:7], s[2:3], 0, v[36:37]
	v_lshlrev_b32_e32 v36, 4, v198
	v_lshl_add_u64 v[40:41], s[0:1], 0, v[36:37]
	v_lshlrev_b32_e32 v36, 5, v198
	s_mov_b64 s[12:13], 0x4f200000
	v_lshl_add_u64 v[42:43], s[4:5], 0, v[36:37]
	v_lshlrev_b32_e32 v36, 3, v198
	v_lshl_add_u64 v[38:39], v[6:7], 0, s[12:13]
	v_lshl_add_u64 v[6:7], s[2:3], 0, v[36:37]
	s_mov_b64 s[4:5], 0x74800000
	v_lshl_add_u64 v[44:45], v[6:7], 0, s[4:5]
	s_mov_b64 s[4:5], 0x1000
	v_lshl_add_u64 v[46:47], v[42:43], 0, s[4:5]
	s_mov_b64 s[4:5], 0x1800
	v_lshl_add_u64 v[48:49], v[42:43], 0, s[4:5]
	global_load_dwordx4 v[120:123], v[42:43], off
	global_load_dwordx4 v[124:127], v[42:43], off offset:16
	global_load_dwordx4 v[200:203], v[42:43], off offset:2048
	global_load_dwordx4 v[204:207], v[42:43], off offset:2064
	global_load_dwordx4 v[208:211], v[46:47], off
	global_load_dwordx4 v[236:239], v[46:47], off offset:16
	global_load_dwordx4 v[240:243], v[48:49], off
	global_load_dwordx4 v[244:247], v[48:49], off offset:16
	s_waitcnt vmcnt(0)
	s_add_u32 s4, s2, 0x74200000
	v_writelane_b32 v252, s95, 53
	s_addc_u32 s5, s3, 0
	v_lshlrev_b32_e32 v2, 2, v0
	v_cmp_eq_u32_e64 s[10:11], 0, v3
	v_mov_b32_e32 v3, v37
	v_writelane_b32 v252, s4, 47
	v_add_u32_e32 v1, 0, v2
	v_lshl_add_u64 v[52:53], s[2:3], 0, v[2:3]
	v_writelane_b32 v252, s5, 48
	s_add_u32 s4, s2, 0x74300000
	v_lshrrev_b32_e32 v2, 2, v0
	v_cndmask_b32_e32 v4, v4, v5, vcc
	v_and_b32_e32 v8, 31, v0
	s_addc_u32 s5, s3, 0
	v_and_b32_e32 v36, 8, v2
	v_lshlrev_b32_e32 v64, 2, v4
	v_lshlrev_b32_e32 v4, 2, v8
	v_mov_b32_e32 v5, v37
	v_writelane_b32 v252, s4, 49
	v_lshl_add_u64 v[2:3], s[0:1], 0, v[36:37]
	v_lshrrev_b32_e32 v6, 5, v0
	v_writelane_b32 v252, s5, 50
	s_add_u32 s4, s2, 0x74400000
	v_lshl_add_u64 v[54:55], v[2:3], 0, 32
	v_lshl_add_u64 v[2:3], s[2:3], 0, v[4:5]
	s_mov_b64 s[0:1], 0x38100000
	s_addc_u32 s5, s3, 0
	v_lshl_add_u64 v[56:57], v[2:3], 0, s[0:1]
	v_mul_u32_u24_e32 v2, 0x84, v6
	v_lshrrev_b32_e32 v35, 3, v0
	v_lshlrev_b32_e32 v9, 7, v0
	v_lshl_add_u64 v[50:51], s[6:7], 0, v[4:5]
	v_writelane_b32 v252, s4, 51
	s_add_u32 s6, s2, 0x78800000
	v_add3_u32 v2, v2, v4, 0
	v_cmp_gt_u32_e64 s[8:9], 32, v0
	s_mov_b32 s95, 0
	v_lshl_add_u32 v65, v35, 2, 0
	v_and_b32_e32 v66, 4, v35
	v_add_u32_e32 v34, 0, v4
	v_writelane_b32 v252, s5, 52
	s_addc_u32 s7, s3, 0
	v_lshl_or_b32 v67, s14, 6, v8
	s_lshl_b32 s33, s80, 6
	v_or_b32_e32 v68, 0xfffffe00, v0
	v_add_u32_e32 v69, 0x100, v2
	v_lshl_add_u32 v70, v6, 2, 0
	v_mov_b32_e32 v71, 0x358637bd
	v_mov_b32_e32 v72, 0x260
	v_add_u32_e32 v73, v1, v9
	v_mov_b32_e32 v74, 1
	s_mov_b32 s89, 0x3fb8aa3b
	s_mov_b32 s84, 0xc2ce8ed0
	s_mov_b32 s85, 0x42b17218
	v_mov_b32_e32 v75, 0xff61b1e6
	v_mov_b32_e32 v76, 0x7f800000
	s_mov_b32 s88, s14
	s_mov_b32 s4, s14
	s_branch .LBB0_985

.LBB0_989:
	s_or_b64 exec, exec, s[2:3]
	s_andn2_b64 vcc, exec, s[90:91]
	s_lshr_b32 s0, s1, 6
	s_cbranch_vccnz .LBB0_991
	s_lshl_b32 s2, s0, 3
	s_add_i32 s12, s2, s5
	s_ashr_i32 s13, s12, 31
	s_lshl_b64 s[2:3], s[12:13], 12
	v_lshl_add_u64 v[22:23], v[40:41], 0, s[2:3]
	s_waitcnt lgkmcnt(0)
	s_barrier
	s_waitcnt vmcnt(0)
	global_load_dwordx4 v[10:13], v[22:23], off
	v_mov_b64_e32 v[18:19], v[120:121]
	v_mov_b64_e32 v[20:21], v[122:123]
	v_mov_b64_e32 v[14:15], v[124:125]
	v_mov_b64_e32 v[16:17], v[126:127]
	s_lshl_b32 s2, s0, 5
	s_add_i32 s2, s2, 0
	v_mov_b32_e32 v2, s2
	ds_read_b128 v[6:9], v2
	ds_read_b128 v[2:5], v2 offset:16
	v_mov_b32_e32 v24, v37
	v_mov_b32_e32 v25, v37
	s_add_i32 s14, s12, 1
	s_ashr_i32 s15, s14, 31
	s_lshl_b64 s[16:17], s[12:13], 11
	s_lshl_b64 s[2:3], s[14:15], 12
	v_lshl_add_u64 v[86:87], v[44:45], 0, s[16:17]
	global_load_dwordx4 v[26:29], v[22:23], off offset:1024
	global_load_dwordx4 v[30:33], v[22:23], off offset:2048
	global_load_dwordx4 v[58:61], v[22:23], off offset:3072
	v_lshl_add_u64 v[22:23], v[40:41], 0, s[2:3]
	v_mov_b32_e32 v88, v37
	v_mov_b32_e32 v89, v37
	s_add_i32 s2, s12, 2
	s_ashr_i32 s3, s2, 31
	s_lshl_b64 s[16:17], s[2:3], 12
	s_lshl_b64 s[14:15], s[14:15], 11
	s_lshl_b64 s[2:3], s[2:3], 11
	s_waitcnt vmcnt(3)
	v_lshlrev_b32_e32 v36, 16, v10
	v_and_b32_e32 v10, 0xffff0000, v10
	v_lshlrev_b32_e32 v78, 16, v12
	v_and_b32_e32 v12, 0xffff0000, v12
	s_waitcnt lgkmcnt(1)
	v_mul_f32_e32 v36, v6, v36
	v_mul_f32_e32 v10, v6, v10
	v_mul_f32_e32 v78, v6, v78
	v_mul_f32_e32 v12, v6, v12
	v_mul_f32_e32 v18, v36, v18
	v_mul_f32_e32 v10, v10, v19
	v_mul_f32_e32 v14, v78, v14
	v_mul_f32_e32 v12, v12, v15
	v_cvt_pk_fp8_f32 v24, v18, v10
	v_cvt_pk_fp8_f32 v25, v14, v12
	v_lshlrev_b32_e32 v77, 16, v11
	v_and_b32_e32 v11, 0xffff0000, v11
	v_lshlrev_b32_e32 v79, 16, v13
	v_and_b32_e32 v13, 0xffff0000, v13
	v_mul_f32_e32 v77, v6, v77
	v_mul_f32_e32 v11, v6, v11
	v_mul_f32_e32 v79, v6, v79
	v_mul_f32_e32 v13, v6, v13
	v_mul_f32_e32 v19, v77, v20
	v_mul_f32_e32 v11, v11, v21
	v_mul_f32_e32 v10, v79, v16
	v_mul_f32_e32 v12, v13, v17
	v_cvt_pk_fp8_f32 v24, v19, v11 op_sel:[0,0,1]
	v_cvt_pk_fp8_f32 v25, v10, v12 op_sel:[0,0,1]
	global_load_dwordx4 v[10:13], v[22:23], off
	global_load_dwordx4 v[14:17], v[22:23], off offset:1024
	global_load_dwordx4 v[18:21], v[22:23], off offset:2048
	global_load_dwordx4 v[78:81], v[22:23], off offset:3072
	s_waitcnt vmcnt(6)
	v_lshlrev_b32_e32 v36, 16, v26
	v_and_b32_e32 v26, 0xffff0000, v26
	global_store_dwordx2 v[86:87], v[24:25], off
	v_mov_b64_e32 v[22:23], v[200:201]
	v_mov_b64_e32 v[24:25], v[202:203]
	s_nop 0
	v_mov_b64_e32 v[82:83], v[204:205]
	v_mov_b64_e32 v[84:85], v[206:207]
	v_lshlrev_b32_e32 v77, 16, v27
	v_and_b32_e32 v27, 0xffff0000, v27
	v_lshlrev_b32_e32 v90, 16, v28
	v_and_b32_e32 v28, 0xffff0000, v28
	v_mul_f32_e32 v36, v6, v36
	v_mul_f32_e32 v26, v6, v26
	v_mul_f32_e32 v27, v6, v27
	v_mul_f32_e32 v90, v6, v90
	v_mul_f32_e32 v28, v6, v28
	v_lshlrev_b32_e32 v91, 16, v29
	v_and_b32_e32 v29, 0xffff0000, v29
	v_mul_f32_e32 v77, v6, v77
	v_mul_f32_e32 v91, v6, v91
	v_mul_f32_e32 v29, v6, v29
	v_mul_f32_e32 v22, v36, v22
	v_mul_f32_e32 v23, v26, v23
	v_mul_f32_e32 v25, v27, v25
	v_mul_f32_e32 v26, v90, v82
	v_mul_f32_e32 v27, v28, v83
	v_cvt_pk_fp8_f32 v88, v22, v23
	v_cvt_pk_fp8_f32 v89, v26, v27
	v_mul_f32_e32 v24, v77, v24
	v_mul_f32_e32 v22, v91, v84
	v_mul_f32_e32 v23, v29, v85
	v_cvt_pk_fp8_f32 v88, v24, v25 op_sel:[0,0,1]
	v_cvt_pk_fp8_f32 v89, v22, v23 op_sel:[0,0,1]
	s_waitcnt vmcnt(6)
	v_lshlrev_b32_e32 v36, 16, v30
	v_and_b32_e32 v30, 0xffff0000, v30
	v_lshlrev_b32_e32 v84, 16, v32
	global_store_dwordx2 v[86:87], v[88:89], off offset:512
	v_mov_b64_e32 v[22:23], v[208:209]
	v_mov_b64_e32 v[24:25], v[210:211]
	v_mov_b64_e32 v[26:27], v[236:237]
	v_mov_b64_e32 v[28:29], v[238:239]
	v_and_b32_e32 v32, 0xffff0000, v32
	v_mul_f32_e32 v36, v6, v36
	v_mul_f32_e32 v30, v6, v30
	v_mul_f32_e32 v84, v6, v84
	v_mul_f32_e32 v32, v6, v32
	v_mov_b32_e32 v82, v37
	v_mov_b32_e32 v83, v37
	v_lshlrev_b32_e32 v77, 16, v31
	v_and_b32_e32 v31, 0xffff0000, v31
	v_lshlrev_b32_e32 v85, 16, v33
	v_and_b32_e32 v33, 0xffff0000, v33
	v_mul_f32_e32 v77, v6, v77
	v_mul_f32_e32 v31, v6, v31
	v_mul_f32_e32 v85, v6, v85
	v_mul_f32_e32 v33, v6, v33
	v_mov_b32_e32 v88, v37
	v_mov_b32_e32 v89, v37
	s_waitcnt vmcnt(4)
	v_lshlrev_b32_e32 v90, 16, v17
	v_and_b32_e32 v17, 0xffff0000, v17
	v_mul_f32_e32 v90, v7, v90
	v_mul_f32_e32 v17, v7, v17
	v_mul_f32_e32 v22, v36, v22
	v_mul_f32_e32 v23, v30, v23
	v_mul_f32_e32 v26, v84, v26
	v_mul_f32_e32 v27, v32, v27
	v_cvt_pk_fp8_f32 v82, v22, v23
	v_cvt_pk_fp8_f32 v83, v26, v27
	v_mul_f32_e32 v24, v77, v24
	v_mul_f32_e32 v25, v31, v25
	v_mul_f32_e32 v22, v85, v28
	v_mul_f32_e32 v23, v33, v29
	v_cvt_pk_fp8_f32 v82, v24, v25 op_sel:[0,0,1]
	v_cvt_pk_fp8_f32 v83, v22, v23 op_sel:[0,0,1]
	v_lshlrev_b32_e32 v32, 16, v58
	v_and_b32_e32 v33, 0xffff0000, v58
	v_lshlrev_b32_e32 v36, 16, v59
	global_store_dwordx2 v[86:87], v[82:83], off offset:1024
	v_mov_b64_e32 v[22:23], v[240:241]
	v_mov_b64_e32 v[24:25], v[242:243]
	v_mov_b64_e32 v[26:27], v[244:245]
	v_mov_b64_e32 v[28:29], v[246:247]
	v_and_b32_e32 v58, 0xffff0000, v59
	v_lshlrev_b32_e32 v59, 16, v60
	v_and_b32_e32 v60, 0xffff0000, v60
	v_mul_f32_e32 v32, v6, v32
	v_mul_f32_e32 v33, v6, v33
	v_mul_f32_e32 v59, v6, v59
	v_mul_f32_e32 v60, v6, v60
	v_mov_b32_e32 v30, v37
	v_mov_b32_e32 v31, v37
	v_lshlrev_b32_e32 v77, 16, v61
	v_and_b32_e32 v61, 0xffff0000, v61
	v_mul_f32_e32 v36, v6, v36
	v_mul_f32_e32 v58, v6, v58
	v_mul_f32_e32 v77, v6, v77
	v_mul_f32_e32 v6, v6, v61
	v_mul_f32_e32 v22, v32, v22
	v_mul_f32_e32 v23, v33, v23
	v_mul_f32_e32 v26, v59, v26
	v_mul_f32_e32 v27, v60, v27
	v_cvt_pk_fp8_f32 v30, v22, v23
	v_cvt_pk_fp8_f32 v31, v26, v27
	v_mul_f32_e32 v24, v36, v24
	v_mul_f32_e32 v25, v58, v25
	v_mul_f32_e32 v22, v77, v28
	v_mul_f32_e32 v6, v6, v29
	v_cvt_pk_fp8_f32 v30, v24, v25 op_sel:[0,0,1]
	v_cvt_pk_fp8_f32 v31, v22, v6 op_sel:[0,0,1]
	v_lshlrev_b32_e32 v6, 16, v10
	v_and_b32_e32 v10, 0xffff0000, v10
	v_lshlrev_b32_e32 v33, 16, v12
	global_store_dwordx2 v[86:87], v[30:31], off offset:1536
	v_mov_b64_e32 v[22:23], v[120:121]
	v_mov_b64_e32 v[24:25], v[122:123]
	v_mov_b64_e32 v[26:27], v[124:125]
	v_mov_b64_e32 v[28:29], v[126:127]
	v_and_b32_e32 v12, 0xffff0000, v12
	v_mul_f32_e32 v6, v7, v6
	v_mul_f32_e32 v10, v7, v10
	v_mul_f32_e32 v33, v7, v33
	v_mul_f32_e32 v12, v7, v12
	v_mov_b32_e32 v58, v37
	v_mov_b32_e32 v59, v37
	v_lshlrev_b32_e32 v32, 16, v11
	v_and_b32_e32 v11, 0xffff0000, v11
	v_lshlrev_b32_e32 v36, 16, v13
	v_and_b32_e32 v13, 0xffff0000, v13
	v_mul_f32_e32 v32, v7, v32
	v_mul_f32_e32 v11, v7, v11
	v_mul_f32_e32 v36, v7, v36
	v_mul_f32_e32 v13, v7, v13
	v_lshl_add_u64 v[30:31], v[40:41], 0, s[16:17]
	v_lshl_add_u64 v[86:87], v[44:45], 0, s[14:15]
	v_lshlrev_b32_e32 v77, 16, v16
	v_and_b32_e32 v16, 0xffff0000, v16
	v_mul_f32_e32 v77, v7, v77
	v_mul_f32_e32 v16, v7, v16
	s_add_i32 s14, s12, 3
	s_ashr_i32 s15, s14, 31
	s_lshl_b64 s[16:17], s[14:15], 12
	s_lshl_b64 s[14:15], s[14:15], 11
	v_mul_f32_e32 v6, v6, v22
	v_mul_f32_e32 v10, v10, v23
	v_mul_f32_e32 v23, v33, v26
	v_mul_f32_e32 v12, v12, v27
	v_cvt_pk_fp8_f32 v58, v6, v10
	v_cvt_pk_fp8_f32 v59, v23, v12
	v_mul_f32_e32 v22, v32, v24
	v_mul_f32_e32 v11, v11, v25
	v_mul_f32_e32 v6, v36, v28
	v_mul_f32_e32 v10, v13, v29
	v_cvt_pk_fp8_f32 v58, v22, v11 op_sel:[0,0,1]
	v_cvt_pk_fp8_f32 v59, v6, v10 op_sel:[0,0,1]
	global_load_dwordx4 v[10:13], v[30:31], off offset:3072
	global_load_dwordx4 v[22:25], v[30:31], off offset:2048
	global_load_dwordx4 v[26:29], v[30:31], off offset:1024
	s_nop 0
	global_load_dwordx4 v[30:33], v[30:31], off
	v_lshlrev_b32_e32 v6, 16, v14
	v_and_b32_e32 v14, 0xffff0000, v14
	global_store_dwordx2 v[86:87], v[58:59], off
	v_mov_b64_e32 v[58:59], v[200:201]
	v_mov_b64_e32 v[60:61], v[202:203]
	s_nop 0
	v_mov_b64_e32 v[82:83], v[204:205]
	v_mov_b64_e32 v[84:85], v[206:207]
	v_mul_f32_e32 v6, v7, v6
	v_mul_f32_e32 v14, v7, v14
	v_lshlrev_b32_e32 v36, 16, v15
	v_and_b32_e32 v15, 0xffff0000, v15
	v_mul_f32_e32 v36, v7, v36
	v_mul_f32_e32 v15, v7, v15
	v_mul_f32_e32 v6, v6, v58
	v_mul_f32_e32 v14, v14, v59
	v_mul_f32_e32 v58, v77, v82
	v_mul_f32_e32 v16, v16, v83
	v_cvt_pk_fp8_f32 v88, v6, v14
	v_cvt_pk_fp8_f32 v89, v58, v16
	v_mul_f32_e32 v36, v36, v60
	v_mul_f32_e32 v15, v15, v61
	v_mul_f32_e32 v6, v90, v84
	v_mul_f32_e32 v14, v17, v85
	v_cvt_pk_fp8_f32 v88, v36, v15 op_sel:[0,0,1]
	v_cvt_pk_fp8_f32 v89, v6, v14 op_sel:[0,0,1]
	s_waitcnt vmcnt(10)
	v_lshlrev_b32_e32 v6, 16, v18
	v_and_b32_e32 v18, 0xffff0000, v18
	v_lshlrev_b32_e32 v36, 16, v19
	global_store_dwordx2 v[86:87], v[88:89], off offset:512
	v_mov_b64_e32 v[14:15], v[208:209]
	v_mov_b64_e32 v[16:17], v[210:211]
	v_mov_b64_e32 v[58:59], v[236:237]
	v_mov_b64_e32 v[60:61], v[238:239]
	v_and_b32_e32 v19, 0xffff0000, v19
	v_lshlrev_b32_e32 v77, 16, v20
	v_and_b32_e32 v20, 0xffff0000, v20
	v_mul_f32_e32 v6, v7, v6
	v_mul_f32_e32 v18, v7, v18
	v_mul_f32_e32 v36, v7, v36
	v_mul_f32_e32 v19, v7, v19
	v_mul_f32_e32 v77, v7, v77
	v_mul_f32_e32 v20, v7, v20
	v_mov_b32_e32 v82, v37
	v_mov_b32_e32 v83, v37
	v_lshlrev_b32_e32 v84, 16, v21
	v_and_b32_e32 v21, 0xffff0000, v21
	v_mul_f32_e32 v84, v7, v84
	v_mul_f32_e32 v21, v7, v21
	s_waitcnt vmcnt(3)
	v_lshlrev_b32_e32 v88, 16, v28
	v_and_b32_e32 v28, 0xffff0000, v28
	v_mul_f32_e32 v88, v8, v88
	v_mul_f32_e32 v28, v8, v28
	v_lshlrev_b32_e32 v89, 16, v29
	v_and_b32_e32 v29, 0xffff0000, v29
	v_mul_f32_e32 v89, v8, v89
	v_mul_f32_e32 v29, v8, v29
	v_mul_f32_e32 v6, v6, v14
	v_mul_f32_e32 v14, v18, v15
	v_mul_f32_e32 v15, v36, v16
	v_mul_f32_e32 v16, v19, v17
	v_mul_f32_e32 v17, v77, v58
	v_mul_f32_e32 v18, v20, v59
	v_cvt_pk_fp8_f32 v82, v6, v14
	v_cvt_pk_fp8_f32 v83, v17, v18
	v_mul_f32_e32 v6, v84, v60
	v_mul_f32_e32 v14, v21, v61
	v_cvt_pk_fp8_f32 v82, v15, v16 op_sel:[0,0,1]
	v_cvt_pk_fp8_f32 v83, v6, v14 op_sel:[0,0,1]
	v_lshlrev_b32_e32 v6, 16, v78
	v_and_b32_e32 v36, 0xffff0000, v78
	v_lshlrev_b32_e32 v60, 16, v79
	global_store_dwordx2 v[86:87], v[82:83], off offset:1024
	v_mov_b64_e32 v[14:15], v[240:241]
	v_mov_b64_e32 v[16:17], v[242:243]
	v_mov_b64_e32 v[18:19], v[244:245]
	v_mov_b64_e32 v[20:21], v[246:247]
	v_and_b32_e32 v61, 0xffff0000, v79
	v_lshlrev_b32_e32 v77, 16, v80
	v_and_b32_e32 v78, 0xffff0000, v80
	v_mul_f32_e32 v6, v7, v6
	v_mul_f32_e32 v36, v7, v36
	v_mul_f32_e32 v60, v7, v60
	v_mul_f32_e32 v61, v7, v61
	v_mul_f32_e32 v77, v7, v77
	v_mul_f32_e32 v78, v7, v78
	v_mov_b32_e32 v58, v37
	v_mov_b32_e32 v59, v37
	v_lshlrev_b32_e32 v79, 16, v81
	v_and_b32_e32 v80, 0xffff0000, v81
	v_mul_f32_e32 v79, v7, v79
	v_mul_f32_e32 v7, v7, v80
	v_mul_f32_e32 v6, v6, v14
	v_mul_f32_e32 v14, v36, v15
	v_mul_f32_e32 v15, v60, v16
	v_mul_f32_e32 v16, v61, v17
	v_mul_f32_e32 v17, v77, v18
	v_mul_f32_e32 v18, v78, v19
	v_cvt_pk_fp8_f32 v58, v6, v14
	v_cvt_pk_fp8_f32 v59, v17, v18
	v_mul_f32_e32 v6, v79, v20
	v_mul_f32_e32 v7, v7, v21
	v_cvt_pk_fp8_f32 v58, v15, v16 op_sel:[0,0,1]
	v_cvt_pk_fp8_f32 v59, v6, v7 op_sel:[0,0,1]
	s_waitcnt vmcnt(3)
	v_lshlrev_b32_e32 v36, 16, v30
	v_and_b32_e32 v30, 0xffff0000, v30
	v_mul_f32_e32 v36, v8, v36
	global_store_dwordx2 v[86:87], v[58:59], off offset:1536
	v_mov_b64_e32 v[14:15], v[120:121]
	v_mov_b64_e32 v[16:17], v[122:123]
	v_mov_b64_e32 v[18:19], v[124:125]
	v_mov_b64_e32 v[20:21], v[126:127]
	v_lshlrev_b32_e32 v59, 16, v32
	v_and_b32_e32 v32, 0xffff0000, v32
	v_mul_f32_e32 v30, v8, v30
	v_mul_f32_e32 v59, v8, v59
	v_mul_f32_e32 v32, v8, v32
	v_mov_b32_e32 v6, v37
	v_mov_b32_e32 v7, v37
	v_lshlrev_b32_e32 v58, 16, v31
	v_and_b32_e32 v31, 0xffff0000, v31
	v_lshlrev_b32_e32 v60, 16, v33
	v_and_b32_e32 v33, 0xffff0000, v33
	v_mul_f32_e32 v58, v8, v58
	v_mul_f32_e32 v31, v8, v31
	v_mul_f32_e32 v60, v8, v60
	v_mul_f32_e32 v33, v8, v33
	v_lshl_add_u64 v[78:79], v[40:41], 0, s[16:17]
	v_lshl_add_u64 v[86:87], v[44:45], 0, s[2:3]
	v_lshlrev_b32_e32 v77, 16, v27
	v_and_b32_e32 v27, 0xffff0000, v27
	v_mul_f32_e32 v27, v8, v27
	v_mul_f32_e32 v77, v8, v77
	s_add_i32 s2, s12, 4
	s_ashr_i32 s3, s2, 31
	s_lshl_b64 s[16:17], s[2:3], 12
	s_lshl_b64 s[2:3], s[2:3], 11
	v_mul_f32_e32 v14, v36, v14
	v_mul_f32_e32 v15, v30, v15
	v_mul_f32_e32 v18, v59, v18
	v_mul_f32_e32 v19, v32, v19
	v_cvt_pk_fp8_f32 v6, v14, v15
	v_cvt_pk_fp8_f32 v7, v18, v19
	v_mul_f32_e32 v16, v58, v16
	v_mul_f32_e32 v17, v31, v17
	v_mul_f32_e32 v14, v60, v20
	v_mul_f32_e32 v15, v33, v21
	v_cvt_pk_fp8_f32 v6, v16, v17 op_sel:[0,0,1]
	v_cvt_pk_fp8_f32 v7, v14, v15 op_sel:[0,0,1]
	global_load_dwordx4 v[14:17], v[78:79], off
	global_load_dwordx4 v[30:33], v[78:79], off offset:1024
	global_load_dwordx4 v[58:61], v[78:79], off offset:2048
	s_nop 0
	global_load_dwordx4 v[78:81], v[78:79], off offset:3072
	v_lshlrev_b32_e32 v36, 16, v26
	v_and_b32_e32 v26, 0xffff0000, v26
	global_store_dwordx2 v[86:87], v[6:7], off
	v_mov_b64_e32 v[18:19], v[200:201]
	v_mov_b64_e32 v[20:21], v[202:203]
	v_mov_b64_e32 v[82:83], v[204:205]
	v_mov_b64_e32 v[84:85], v[206:207]
	v_mul_f32_e32 v36, v8, v36
	v_mul_f32_e32 v26, v8, v26
	v_mov_b32_e32 v6, v37
	v_mov_b32_e32 v7, v37
	v_mul_f32_e32 v18, v36, v18
	v_mul_f32_e32 v19, v26, v19
	v_mul_f32_e32 v21, v27, v21
	v_mul_f32_e32 v26, v88, v82
	v_mul_f32_e32 v27, v28, v83
	v_cvt_pk_fp8_f32 v6, v18, v19
	v_cvt_pk_fp8_f32 v7, v26, v27
	v_mul_f32_e32 v20, v77, v20
	v_mul_f32_e32 v18, v89, v84
	v_mul_f32_e32 v19, v29, v85
	v_cvt_pk_fp8_f32 v6, v20, v21 op_sel:[0,0,1]
	v_cvt_pk_fp8_f32 v7, v18, v19 op_sel:[0,0,1]
	v_lshlrev_b32_e32 v36, 16, v22
	v_and_b32_e32 v22, 0xffff0000, v22
	v_lshlrev_b32_e32 v77, 16, v23
	global_store_dwordx2 v[86:87], v[6:7], off offset:512
	v_mov_b64_e32 v[18:19], v[208:209]
	v_mov_b64_e32 v[20:21], v[210:211]
	v_mov_b64_e32 v[26:27], v[236:237]
	v_mov_b64_e32 v[28:29], v[238:239]
	v_and_b32_e32 v23, 0xffff0000, v23
	v_lshlrev_b32_e32 v82, 16, v24
	v_and_b32_e32 v24, 0xffff0000, v24
	v_mul_f32_e32 v36, v8, v36
	v_mul_f32_e32 v22, v8, v22
	v_mul_f32_e32 v23, v8, v23
	v_mul_f32_e32 v82, v8, v82
	v_mul_f32_e32 v24, v8, v24
	v_mov_b32_e32 v6, v37
	v_mov_b32_e32 v7, v37
	v_lshlrev_b32_e32 v83, 16, v25
	v_and_b32_e32 v25, 0xffff0000, v25
	v_mul_f32_e32 v77, v8, v77
	v_mul_f32_e32 v83, v8, v83
	v_mul_f32_e32 v25, v8, v25
	s_waitcnt vmcnt(4)
	v_lshlrev_b32_e32 v88, 16, v33
	v_and_b32_e32 v33, 0xffff0000, v33
	v_mul_f32_e32 v88, v9, v88
	v_mul_f32_e32 v33, v9, v33
	v_mul_f32_e32 v18, v36, v18
	v_mul_f32_e32 v19, v22, v19
	v_mul_f32_e32 v21, v23, v21
	v_mul_f32_e32 v22, v82, v26
	v_mul_f32_e32 v23, v24, v27
	v_cvt_pk_fp8_f32 v6, v18, v19
	v_cvt_pk_fp8_f32 v7, v22, v23
	v_mul_f32_e32 v20, v77, v20
	v_mul_f32_e32 v18, v83, v28
	v_mul_f32_e32 v19, v25, v29
	v_cvt_pk_fp8_f32 v6, v20, v21 op_sel:[0,0,1]
	v_cvt_pk_fp8_f32 v7, v18, v19 op_sel:[0,0,1]
	v_lshlrev_b32_e32 v26, 16, v10
	v_and_b32_e32 v10, 0xffff0000, v10
	v_lshlrev_b32_e32 v28, 16, v12
	global_store_dwordx2 v[86:87], v[6:7], off offset:1024
	v_mov_b64_e32 v[18:19], v[240:241]
	v_mov_b64_e32 v[20:21], v[242:243]
	v_mov_b64_e32 v[22:23], v[244:245]
	v_mov_b64_e32 v[24:25], v[246:247]
	v_and_b32_e32 v12, 0xffff0000, v12
	v_lshlrev_b32_e32 v27, 16, v11
	v_and_b32_e32 v11, 0xffff0000, v11
	v_lshlrev_b32_e32 v29, 16, v13
	v_and_b32_e32 v13, 0xffff0000, v13
	v_mul_f32_e32 v26, v8, v26
	v_mul_f32_e32 v10, v8, v10
	v_mul_f32_e32 v28, v8, v28
	v_mul_f32_e32 v12, v8, v12
	v_mov_b32_e32 v6, v37
	v_mov_b32_e32 v7, v37
	v_mul_f32_e32 v27, v8, v27
	v_mul_f32_e32 v11, v8, v11
	v_mul_f32_e32 v29, v8, v29
	v_mul_f32_e32 v8, v8, v13
	v_lshlrev_b32_e32 v36, 16, v31
	v_and_b32_e32 v31, 0xffff0000, v31
	v_lshlrev_b32_e32 v77, 16, v32
	v_and_b32_e32 v32, 0xffff0000, v32
	v_mul_f32_e32 v36, v9, v36
	v_mul_f32_e32 v31, v9, v31
	v_mul_f32_e32 v77, v9, v77
	v_mul_f32_e32 v32, v9, v32
	v_mul_f32_e32 v13, v26, v18
	v_mul_f32_e32 v10, v10, v19
	v_mul_f32_e32 v19, v28, v22
	v_mul_f32_e32 v12, v12, v23
	v_cvt_pk_fp8_f32 v6, v13, v10
	v_cvt_pk_fp8_f32 v7, v19, v12
	v_mul_f32_e32 v18, v27, v20
	v_mul_f32_e32 v11, v11, v21
	v_mul_f32_e32 v10, v29, v24
	v_mul_f32_e32 v8, v8, v25
	v_cvt_pk_fp8_f32 v6, v18, v11 op_sel:[0,0,1]
	v_cvt_pk_fp8_f32 v7, v10, v8 op_sel:[0,0,1]
	v_lshlrev_b32_e32 v8, 16, v14
	v_and_b32_e32 v14, 0xffff0000, v14
	v_lshlrev_b32_e32 v24, 16, v15
	global_store_dwordx2 v[86:87], v[6:7], off offset:1536
	v_mov_b64_e32 v[10:11], v[120:121]
	v_mov_b64_e32 v[12:13], v[122:123]
	v_mov_b64_e32 v[18:19], v[124:125]
	v_mov_b64_e32 v[20:21], v[126:127]
	v_and_b32_e32 v15, 0xffff0000, v15
	v_lshlrev_b32_e32 v25, 16, v16
	v_and_b32_e32 v16, 0xffff0000, v16
	v_mul_f32_e32 v8, v9, v8
	v_mul_f32_e32 v14, v9, v14
	v_mul_f32_e32 v24, v9, v24
	v_mul_f32_e32 v15, v9, v15
	v_mul_f32_e32 v25, v9, v25
	v_mul_f32_e32 v16, v9, v16
	v_mov_b32_e32 v6, v37
	v_mov_b32_e32 v7, v37
	v_lshlrev_b32_e32 v26, 16, v17
	v_and_b32_e32 v17, 0xffff0000, v17
	v_mul_f32_e32 v26, v9, v26
	v_mul_f32_e32 v17, v9, v17
	v_lshl_add_u64 v[22:23], v[40:41], 0, s[16:17]
	v_lshl_add_u64 v[86:87], v[44:45], 0, s[14:15]
	s_add_i32 s14, s12, 5
	s_ashr_i32 s15, s14, 31
	s_lshl_b64 s[16:17], s[14:15], 12
	s_lshl_b64 s[14:15], s[14:15], 11
	v_mul_f32_e32 v8, v8, v10
	v_mul_f32_e32 v10, v14, v11
	v_mul_f32_e32 v11, v24, v12
	v_mul_f32_e32 v12, v15, v13
	v_mul_f32_e32 v13, v25, v18
	v_mul_f32_e32 v14, v16, v19
	v_cvt_pk_fp8_f32 v6, v8, v10
	v_cvt_pk_fp8_f32 v7, v13, v14
	v_mul_f32_e32 v8, v26, v20
	v_mul_f32_e32 v10, v17, v21
	v_cvt_pk_fp8_f32 v6, v11, v12 op_sel:[0,0,1]
	v_cvt_pk_fp8_f32 v7, v8, v10 op_sel:[0,0,1]
	global_load_dwordx4 v[10:13], v[22:23], off offset:3072
	global_load_dwordx4 v[18:21], v[22:23], off offset:2048
	global_load_dwordx4 v[82:85], v[22:23], off offset:1024
	global_load_dwordx4 v[14:17], v[22:23], off
	v_lshlrev_b32_e32 v8, 16, v30
	v_and_b32_e32 v30, 0xffff0000, v30
	global_store_dwordx2 v[86:87], v[6:7], off
	v_mov_b64_e32 v[22:23], v[200:201]
	v_mov_b64_e32 v[24:25], v[202:203]
	v_mov_b64_e32 v[26:27], v[204:205]
	v_mov_b64_e32 v[28:29], v[206:207]
	v_mul_f32_e32 v8, v9, v8
	v_mul_f32_e32 v30, v9, v30
	v_mov_b32_e32 v6, v37
	v_mov_b32_e32 v7, v37
	v_mul_f32_e32 v8, v8, v22
	v_mul_f32_e32 v22, v30, v23
	v_mul_f32_e32 v23, v36, v24
	v_mul_f32_e32 v24, v31, v25
	v_mul_f32_e32 v25, v77, v26
	v_mul_f32_e32 v26, v32, v27
	v_cvt_pk_fp8_f32 v6, v8, v22
	v_cvt_pk_fp8_f32 v7, v25, v26
	v_mul_f32_e32 v8, v88, v28
	v_mul_f32_e32 v22, v33, v29
	v_cvt_pk_fp8_f32 v6, v23, v24 op_sel:[0,0,1]
	v_cvt_pk_fp8_f32 v7, v8, v22 op_sel:[0,0,1]
	s_waitcnt vmcnt(10)
	v_lshlrev_b32_e32 v8, 16, v58
	v_and_b32_e32 v30, 0xffff0000, v58
	v_lshlrev_b32_e32 v31, 16, v59
	global_store_dwordx2 v[86:87], v[6:7], off offset:512
	v_mov_b64_e32 v[22:23], v[208:209]
	v_mov_b64_e32 v[24:25], v[210:211]
	v_mov_b64_e32 v[26:27], v[236:237]
	v_mov_b64_e32 v[28:29], v[238:239]
	v_and_b32_e32 v32, 0xffff0000, v59
	v_lshlrev_b32_e32 v33, 16, v60
	v_and_b32_e32 v36, 0xffff0000, v60
	v_mul_f32_e32 v8, v9, v8
	v_mul_f32_e32 v30, v9, v30
	v_mul_f32_e32 v31, v9, v31
	v_mul_f32_e32 v32, v9, v32
	v_mul_f32_e32 v33, v9, v33
	v_mul_f32_e32 v36, v9, v36
	v_mov_b32_e32 v6, v37
	v_mov_b32_e32 v7, v37
	v_lshlrev_b32_e32 v58, 16, v61
	v_and_b32_e32 v59, 0xffff0000, v61
	v_mul_f32_e32 v58, v9, v58
	v_mul_f32_e32 v59, v9, v59
	s_waitcnt vmcnt(3)
	v_and_b32_e32 v77, 0xffff0000, v82
	s_waitcnt lgkmcnt(0)
	v_mul_f32_e32 v77, v2, v77
	v_mul_f32_e32 v8, v8, v22
	v_mul_f32_e32 v22, v30, v23
	v_mul_f32_e32 v23, v31, v24
	v_mul_f32_e32 v24, v32, v25
	v_mul_f32_e32 v25, v33, v26
	v_mul_f32_e32 v26, v36, v27
	v_cvt_pk_fp8_f32 v6, v8, v22
	v_cvt_pk_fp8_f32 v7, v25, v26
	v_mul_f32_e32 v8, v58, v28
	v_mul_f32_e32 v22, v59, v29
	v_cvt_pk_fp8_f32 v6, v23, v24 op_sel:[0,0,1]
	v_cvt_pk_fp8_f32 v7, v8, v22 op_sel:[0,0,1]
	v_lshlrev_b32_e32 v8, 16, v78
	v_and_b32_e32 v30, 0xffff0000, v78
	v_lshlrev_b32_e32 v31, 16, v79
	global_store_dwordx2 v[86:87], v[6:7], off offset:1024
	v_mov_b64_e32 v[22:23], v[240:241]
	v_mov_b64_e32 v[24:25], v[242:243]
	v_mov_b64_e32 v[26:27], v[244:245]
	v_mov_b64_e32 v[28:29], v[246:247]
	v_and_b32_e32 v32, 0xffff0000, v79
	v_lshlrev_b32_e32 v33, 16, v80
	v_and_b32_e32 v36, 0xffff0000, v80
	v_mul_f32_e32 v8, v9, v8
	v_mul_f32_e32 v30, v9, v30
	v_mul_f32_e32 v31, v9, v31
	v_mul_f32_e32 v32, v9, v32
	v_mul_f32_e32 v33, v9, v33
	v_mul_f32_e32 v36, v9, v36
	v_mov_b32_e32 v6, v37
	v_mov_b32_e32 v7, v37
	v_lshlrev_b32_e32 v58, 16, v81
	v_and_b32_e32 v59, 0xffff0000, v81
	v_mul_f32_e32 v58, v9, v58
	v_mul_f32_e32 v9, v9, v59
	v_lshl_add_u64 v[78:79], v[44:45], 0, s[2:3]
	v_mov_b32_e32 v80, v37
	v_mov_b32_e32 v81, v37
	v_mul_f32_e32 v8, v8, v22
	v_mul_f32_e32 v22, v30, v23
	v_mul_f32_e32 v23, v31, v24
	v_mul_f32_e32 v24, v32, v25
	v_mul_f32_e32 v25, v33, v26
	v_mul_f32_e32 v26, v36, v27
	v_cvt_pk_fp8_f32 v6, v8, v22
	v_cvt_pk_fp8_f32 v7, v25, v26
	v_mul_f32_e32 v8, v58, v28
	v_mul_f32_e32 v9, v9, v29
	v_cvt_pk_fp8_f32 v6, v23, v24 op_sel:[0,0,1]
	v_cvt_pk_fp8_f32 v7, v8, v9 op_sel:[0,0,1]
	s_waitcnt vmcnt(3)
	v_lshlrev_b32_e32 v26, 16, v14
	v_and_b32_e32 v14, 0xffff0000, v14
	v_lshlrev_b32_e32 v27, 16, v15
	global_store_dwordx2 v[86:87], v[6:7], off offset:1536
	v_mov_b64_e32 v[6:7], v[120:121]
	v_mov_b64_e32 v[8:9], v[122:123]
	s_nop 0
	v_mov_b64_e32 v[22:23], v[124:125]
	v_mov_b64_e32 v[24:25], v[126:127]
	v_and_b32_e32 v15, 0xffff0000, v15
	v_lshlrev_b32_e32 v28, 16, v16
	v_and_b32_e32 v16, 0xffff0000, v16
	v_mul_f32_e32 v26, v2, v26
	v_mul_f32_e32 v14, v2, v14
	v_mul_f32_e32 v15, v2, v15
	v_mul_f32_e32 v28, v2, v28
	v_mul_f32_e32 v16, v2, v16
	v_mov_b32_e32 v30, v37
	v_mov_b32_e32 v31, v37
	v_lshlrev_b32_e32 v29, 16, v17
	v_and_b32_e32 v17, 0xffff0000, v17
	v_mul_f32_e32 v27, v2, v27
	v_mul_f32_e32 v29, v2, v29
	v_mul_f32_e32 v17, v2, v17
	v_lshl_add_u64 v[32:33], v[40:41], 0, s[16:17]
	v_lshlrev_b32_e32 v36, 16, v82
	v_lshlrev_b32_e32 v86, 16, v84
	v_and_b32_e32 v84, 0xffff0000, v84
	v_mul_f32_e32 v36, v2, v36
	v_mul_f32_e32 v86, v2, v86
	v_mul_f32_e32 v84, v2, v84
	v_lshlrev_b32_e32 v82, 16, v83
	v_and_b32_e32 v83, 0xffff0000, v83
	v_lshlrev_b32_e32 v87, 16, v85
	v_and_b32_e32 v85, 0xffff0000, v85
	v_mul_f32_e32 v82, v2, v82
	v_mul_f32_e32 v83, v2, v83
	v_mul_f32_e32 v87, v2, v87
	v_mul_f32_e32 v85, v2, v85
	s_add_i32 s16, s12, 6
	s_ashr_i32 s17, s16, 31
	s_lshl_b64 s[2:3], s[16:17], 12
	s_add_i32 s12, s12, 7
	s_ashr_i32 s13, s12, 31
	v_mul_f32_e32 v6, v26, v6
	v_mul_f32_e32 v7, v14, v7
	v_mul_f32_e32 v9, v15, v9
	v_mul_f32_e32 v14, v28, v22
	v_mul_f32_e32 v15, v16, v23
	v_cvt_pk_fp8_f32 v30, v6, v7
	v_cvt_pk_fp8_f32 v31, v14, v15
	v_mul_f32_e32 v8, v27, v8
	v_mul_f32_e32 v6, v29, v24
	v_mul_f32_e32 v7, v17, v25
	v_cvt_pk_fp8_f32 v30, v8, v9 op_sel:[0,0,1]
	v_cvt_pk_fp8_f32 v31, v6, v7 op_sel:[0,0,1]
	global_load_dwordx4 v[26:29], v[32:33], off
	global_load_dwordx4 v[22:25], v[32:33], off offset:1024
	global_load_dwordx4 v[14:17], v[32:33], off offset:2048
	global_load_dwordx4 v[6:9], v[32:33], off offset:3072
	s_nop 0
	global_store_dwordx2 v[78:79], v[30:31], off
	v_mov_b64_e32 v[30:31], v[200:201]
	v_mov_b64_e32 v[32:33], v[202:203]
	s_nop 0
	v_mov_b64_e32 v[58:59], v[204:205]
	v_mov_b64_e32 v[60:61], v[206:207]
	v_mul_f32_e32 v30, v36, v30
	v_mul_f32_e32 v31, v77, v31
	v_mul_f32_e32 v36, v86, v58
	v_mul_f32_e32 v58, v84, v59
	v_cvt_pk_fp8_f32 v80, v30, v31
	v_cvt_pk_fp8_f32 v81, v36, v58
	v_mul_f32_e32 v32, v82, v32
	v_mul_f32_e32 v33, v83, v33
	v_mul_f32_e32 v30, v87, v60
	v_mul_f32_e32 v31, v85, v61
	v_cvt_pk_fp8_f32 v80, v32, v33 op_sel:[0,0,1]
	v_cvt_pk_fp8_f32 v81, v30, v31 op_sel:[0,0,1]
	v_lshlrev_b32_e32 v36, 16, v18
	v_and_b32_e32 v18, 0xffff0000, v18
	v_lshlrev_b32_e32 v77, 16, v19
	global_store_dwordx2 v[78:79], v[80:81], off offset:512
	v_mov_b64_e32 v[30:31], v[208:209]
	v_mov_b64_e32 v[32:33], v[210:211]
	v_mov_b64_e32 v[58:59], v[236:237]
	v_mov_b64_e32 v[60:61], v[238:239]
	v_lshlrev_b32_e32 v82, 16, v20
	v_and_b32_e32 v20, 0xffff0000, v20
	v_mul_f32_e32 v36, v2, v36
	v_mul_f32_e32 v18, v2, v18
	v_mul_f32_e32 v77, v2, v77
	v_mul_f32_e32 v82, v2, v82
	v_mul_f32_e32 v20, v2, v20
	v_mov_b32_e32 v80, v37
	v_mov_b32_e32 v81, v37
	v_and_b32_e32 v19, 0xffff0000, v19
	v_lshlrev_b32_e32 v83, 16, v21
	v_and_b32_e32 v21, 0xffff0000, v21
	v_mul_f32_e32 v19, v2, v19
	v_mul_f32_e32 v83, v2, v83
	v_mul_f32_e32 v21, v2, v21
	v_mov_b32_e32 v84, v37
	v_mov_b32_e32 v85, v37
	s_waitcnt vmcnt(4)
	v_lshlrev_b32_e32 v86, 16, v25
	v_and_b32_e32 v25, 0xffff0000, v25
	v_mul_f32_e32 v86, v3, v86
	v_mul_f32_e32 v25, v3, v25
	v_mul_f32_e32 v30, v36, v30
	v_mul_f32_e32 v18, v18, v31
	v_mul_f32_e32 v31, v77, v32
	v_mul_f32_e32 v32, v82, v58
	v_mul_f32_e32 v20, v20, v59
	v_cvt_pk_fp8_f32 v80, v30, v18
	v_cvt_pk_fp8_f32 v81, v32, v20
	v_mul_f32_e32 v19, v19, v33
	v_mul_f32_e32 v18, v83, v60
	v_mul_f32_e32 v20, v21, v61
	v_cvt_pk_fp8_f32 v80, v31, v19 op_sel:[0,0,1]
	v_cvt_pk_fp8_f32 v81, v18, v20 op_sel:[0,0,1]
	v_lshlrev_b32_e32 v36, 16, v10
	v_and_b32_e32 v10, 0xffff0000, v10
	v_lshlrev_b32_e32 v61, 16, v12
	global_store_dwordx2 v[78:79], v[80:81], off offset:1024
	v_mov_b64_e32 v[18:19], v[240:241]
	v_mov_b64_e32 v[20:21], v[242:243]
	v_mov_b64_e32 v[30:31], v[244:245]
	v_mov_b64_e32 v[32:33], v[246:247]
	v_and_b32_e32 v12, 0xffff0000, v12
	v_lshlrev_b32_e32 v60, 16, v11
	v_and_b32_e32 v11, 0xffff0000, v11
	v_lshlrev_b32_e32 v77, 16, v13
	v_and_b32_e32 v13, 0xffff0000, v13
	v_mul_f32_e32 v36, v2, v36
	v_mul_f32_e32 v10, v2, v10
	v_mul_f32_e32 v61, v2, v61
	v_mul_f32_e32 v12, v2, v12
	v_mov_b32_e32 v58, v37
	v_mov_b32_e32 v59, v37
	v_mul_f32_e32 v60, v2, v60
	v_mul_f32_e32 v11, v2, v11
	v_mul_f32_e32 v77, v2, v77
	v_mul_f32_e32 v2, v2, v13
	v_lshl_add_u64 v[82:83], v[44:45], 0, s[14:15]
	s_lshl_b64 s[14:15], s[16:17], 11
	v_mul_f32_e32 v13, v36, v18
	v_mul_f32_e32 v10, v10, v19
	v_mul_f32_e32 v19, v61, v30
	v_mul_f32_e32 v12, v12, v31
	v_cvt_pk_fp8_f32 v58, v13, v10
	v_cvt_pk_fp8_f32 v59, v19, v12
	v_mul_f32_e32 v18, v60, v20
	v_mul_f32_e32 v11, v11, v21
	v_mul_f32_e32 v10, v77, v32
	v_mul_f32_e32 v2, v2, v33
	v_cvt_pk_fp8_f32 v58, v18, v11 op_sel:[0,0,1]
	v_cvt_pk_fp8_f32 v59, v10, v2 op_sel:[0,0,1]
	v_lshlrev_b32_e32 v2, 16, v26
	v_and_b32_e32 v26, 0xffff0000, v26
	v_lshlrev_b32_e32 v30, 16, v27
	global_store_dwordx2 v[78:79], v[58:59], off offset:1536
	v_mov_b64_e32 v[10:11], v[120:121]
	v_mov_b64_e32 v[12:13], v[122:123]
	v_mov_b64_e32 v[18:19], v[124:125]
	v_mov_b64_e32 v[20:21], v[126:127]
	v_and_b32_e32 v27, 0xffff0000, v27
	v_lshlrev_b32_e32 v31, 16, v28
	v_and_b32_e32 v28, 0xffff0000, v28
	v_mul_f32_e32 v2, v3, v2
	v_mul_f32_e32 v26, v3, v26
	v_mul_f32_e32 v30, v3, v30
	v_mul_f32_e32 v27, v3, v27
	v_mul_f32_e32 v31, v3, v31
	v_mul_f32_e32 v28, v3, v28
	v_mov_b32_e32 v58, v37
	v_mov_b32_e32 v59, v37
	v_lshlrev_b32_e32 v32, 16, v29
	v_and_b32_e32 v29, 0xffff0000, v29
	v_mul_f32_e32 v32, v3, v32
	v_mul_f32_e32 v29, v3, v29
	v_lshl_add_u64 v[60:61], v[40:41], 0, s[2:3]
	v_lshlrev_b32_e32 v77, 16, v24
	v_and_b32_e32 v24, 0xffff0000, v24
	v_mul_f32_e32 v77, v3, v77
	v_mul_f32_e32 v24, v3, v24
	v_lshlrev_b32_e32 v36, 16, v23
	v_and_b32_e32 v23, 0xffff0000, v23
	v_mul_f32_e32 v36, v3, v36
	v_mul_f32_e32 v23, v3, v23
	s_lshl_b64 s[2:3], s[12:13], 12
	v_mul_f32_e32 v2, v2, v10
	v_mul_f32_e32 v10, v26, v11
	v_mul_f32_e32 v11, v30, v12
	v_mul_f32_e32 v12, v27, v13
	v_mul_f32_e32 v13, v31, v18
	v_mul_f32_e32 v18, v28, v19
	v_cvt_pk_fp8_f32 v58, v2, v10
	v_cvt_pk_fp8_f32 v59, v13, v18
	v_mul_f32_e32 v2, v32, v20
	v_mul_f32_e32 v10, v29, v21
	v_cvt_pk_fp8_f32 v58, v11, v12 op_sel:[0,0,1]
	v_cvt_pk_fp8_f32 v59, v2, v10 op_sel:[0,0,1]
	global_load_dwordx4 v[30:33], v[60:61], off
	global_load_dwordx4 v[26:29], v[60:61], off offset:1024
	global_load_dwordx4 v[18:21], v[60:61], off offset:2048
	global_load_dwordx4 v[10:13], v[60:61], off offset:3072
	v_lshlrev_b32_e32 v2, 16, v22
	v_and_b32_e32 v22, 0xffff0000, v22
	global_store_dwordx2 v[82:83], v[58:59], off
	v_mov_b64_e32 v[58:59], v[200:201]
	v_mov_b64_e32 v[60:61], v[202:203]
	s_nop 0
	v_mov_b64_e32 v[78:79], v[204:205]
	v_mov_b64_e32 v[80:81], v[206:207]
	v_mul_f32_e32 v2, v3, v2
	v_mul_f32_e32 v22, v3, v22
	v_mul_f32_e32 v2, v2, v58
	v_mul_f32_e32 v22, v22, v59
	v_mul_f32_e32 v58, v77, v78
	v_mul_f32_e32 v24, v24, v79
	v_cvt_pk_fp8_f32 v84, v2, v22
	v_cvt_pk_fp8_f32 v85, v58, v24
	v_mul_f32_e32 v36, v36, v60
	v_mul_f32_e32 v23, v23, v61
	v_mul_f32_e32 v2, v86, v80
	v_mul_f32_e32 v22, v25, v81
	v_cvt_pk_fp8_f32 v84, v36, v23 op_sel:[0,0,1]
	v_cvt_pk_fp8_f32 v85, v2, v22 op_sel:[0,0,1]
	s_waitcnt vmcnt(10)
	v_lshlrev_b32_e32 v2, 16, v14
	v_and_b32_e32 v14, 0xffff0000, v14
	v_lshlrev_b32_e32 v77, 16, v16
	global_store_dwordx2 v[82:83], v[84:85], off offset:512
	v_mov_b64_e32 v[22:23], v[208:209]
	v_mov_b64_e32 v[24:25], v[210:211]
	v_mov_b64_e32 v[58:59], v[236:237]
	v_mov_b64_e32 v[60:61], v[238:239]
	v_and_b32_e32 v16, 0xffff0000, v16
	v_mul_f32_e32 v2, v3, v2
	v_mul_f32_e32 v14, v3, v14
	v_mul_f32_e32 v77, v3, v77
	v_mul_f32_e32 v16, v3, v16
	v_mov_b32_e32 v78, v37
	v_mov_b32_e32 v79, v37
	v_lshlrev_b32_e32 v36, 16, v15
	v_and_b32_e32 v15, 0xffff0000, v15
	v_lshlrev_b32_e32 v80, 16, v17
	v_and_b32_e32 v17, 0xffff0000, v17
	v_mul_f32_e32 v36, v3, v36
	v_mul_f32_e32 v15, v3, v15
	v_mul_f32_e32 v80, v3, v80
	v_mul_f32_e32 v17, v3, v17
	s_waitcnt vmcnt(4)
	v_lshlrev_b32_e32 v84, 16, v28
	v_and_b32_e32 v28, 0xffff0000, v28
	v_mul_f32_e32 v84, v4, v84
	v_mul_f32_e32 v28, v4, v28
	v_lshlrev_b32_e32 v85, 16, v29
	v_and_b32_e32 v29, 0xffff0000, v29
	v_mul_f32_e32 v85, v4, v85
	v_mul_f32_e32 v29, v4, v29
	v_mul_f32_e32 v2, v2, v22
	v_mul_f32_e32 v14, v14, v23
	v_mul_f32_e32 v23, v77, v58
	v_mul_f32_e32 v16, v16, v59
	v_cvt_pk_fp8_f32 v78, v2, v14
	v_cvt_pk_fp8_f32 v79, v23, v16
	v_mul_f32_e32 v22, v36, v24
	v_mul_f32_e32 v15, v15, v25
	v_mul_f32_e32 v2, v80, v60
	v_mul_f32_e32 v14, v17, v61
	v_cvt_pk_fp8_f32 v78, v22, v15 op_sel:[0,0,1]
	v_cvt_pk_fp8_f32 v79, v2, v14 op_sel:[0,0,1]
	v_lshlrev_b32_e32 v2, 16, v6
	v_and_b32_e32 v6, 0xffff0000, v6
	v_lshlrev_b32_e32 v60, 16, v8
	global_store_dwordx2 v[82:83], v[78:79], off offset:1024
	v_mov_b64_e32 v[14:15], v[240:241]
	v_mov_b64_e32 v[16:17], v[242:243]
	v_mov_b64_e32 v[22:23], v[244:245]
	v_mov_b64_e32 v[24:25], v[246:247]
	v_and_b32_e32 v8, 0xffff0000, v8
	v_mul_f32_e32 v2, v3, v2
	v_mul_f32_e32 v6, v3, v6
	v_mul_f32_e32 v60, v3, v60
	v_mul_f32_e32 v8, v3, v8
	v_mov_b32_e32 v58, v37
	v_mov_b32_e32 v59, v37
	v_lshlrev_b32_e32 v36, 16, v7
	v_and_b32_e32 v7, 0xffff0000, v7
	v_lshlrev_b32_e32 v61, 16, v9
	v_and_b32_e32 v9, 0xffff0000, v9
	v_mul_f32_e32 v36, v3, v36
	v_mul_f32_e32 v7, v3, v7
	v_mul_f32_e32 v61, v3, v61
	v_mul_f32_e32 v3, v3, v9
	v_lshlrev_b32_e32 v77, 16, v27
	v_and_b32_e32 v27, 0xffff0000, v27
	v_mul_f32_e32 v77, v4, v77
	v_mul_f32_e32 v27, v4, v27
	v_mul_f32_e32 v2, v2, v14
	v_mul_f32_e32 v6, v6, v15
	v_mul_f32_e32 v14, v60, v22
	v_mul_f32_e32 v8, v8, v23
	v_cvt_pk_fp8_f32 v58, v2, v6
	v_cvt_pk_fp8_f32 v59, v14, v8
	v_mul_f32_e32 v9, v36, v16
	v_mul_f32_e32 v7, v7, v17
	v_mul_f32_e32 v2, v61, v24
	v_mul_f32_e32 v3, v3, v25
	v_cvt_pk_fp8_f32 v58, v9, v7 op_sel:[0,0,1]
	v_cvt_pk_fp8_f32 v59, v2, v3 op_sel:[0,0,1]
	v_lshlrev_b32_e32 v22, 16, v30
	v_and_b32_e32 v23, 0xffff0000, v30
	v_lshlrev_b32_e32 v24, 16, v31
	global_store_dwordx2 v[82:83], v[58:59], off offset:1536
	v_mov_b64_e32 v[6:7], v[120:121]
	v_mov_b64_e32 v[8:9], v[122:123]
	v_mov_b64_e32 v[14:15], v[124:125]
	v_mov_b64_e32 v[16:17], v[126:127]
	v_and_b32_e32 v25, 0xffff0000, v31
	v_lshlrev_b32_e32 v30, 16, v32
	v_and_b32_e32 v31, 0xffff0000, v32
	v_mul_f32_e32 v22, v4, v22
	v_mul_f32_e32 v23, v4, v23
	v_mul_f32_e32 v30, v4, v30
	v_mul_f32_e32 v31, v4, v31
	v_mov_b32_e32 v2, v37
	v_mov_b32_e32 v3, v37
	v_lshlrev_b32_e32 v32, 16, v33
	v_and_b32_e32 v33, 0xffff0000, v33
	v_mul_f32_e32 v24, v4, v24
	v_mul_f32_e32 v25, v4, v25
	v_mul_f32_e32 v32, v4, v32
	v_mul_f32_e32 v33, v4, v33
	v_lshl_add_u64 v[58:59], v[40:41], 0, s[2:3]
	v_lshl_add_u64 v[82:83], v[44:45], 0, s[14:15]
	v_lshlrev_b32_e32 v36, 16, v26
	v_and_b32_e32 v26, 0xffff0000, v26
	v_mul_f32_e32 v36, v4, v36
	v_mul_f32_e32 v26, v4, v26
	s_lshl_b64 s[2:3], s[12:13], 11
	v_mul_f32_e32 v6, v22, v6
	v_mul_f32_e32 v7, v23, v7
	v_mul_f32_e32 v14, v30, v14
	v_mul_f32_e32 v15, v31, v15
	v_cvt_pk_fp8_f32 v2, v6, v7
	v_cvt_pk_fp8_f32 v3, v14, v15
	v_mul_f32_e32 v8, v24, v8
	v_mul_f32_e32 v9, v25, v9
	v_mul_f32_e32 v6, v32, v16
	v_mul_f32_e32 v7, v33, v17
	v_cvt_pk_fp8_f32 v2, v8, v9 op_sel:[0,0,1]
	v_cvt_pk_fp8_f32 v3, v6, v7 op_sel:[0,0,1]
	global_load_dwordx4 v[30:33], v[58:59], off
	global_load_dwordx4 v[22:25], v[58:59], off offset:1024
	global_load_dwordx4 v[14:17], v[58:59], off offset:2048
	global_load_dwordx4 v[6:9], v[58:59], off offset:3072
	s_nop 0
	global_store_dwordx2 v[82:83], v[2:3], off
	v_mov_b64_e32 v[58:59], v[200:201]
	v_mov_b64_e32 v[60:61], v[202:203]
	v_mov_b64_e32 v[78:79], v[204:205]
	v_mov_b64_e32 v[80:81], v[206:207]
	v_mov_b32_e32 v2, v37
	v_mov_b32_e32 v3, v37
	v_mul_f32_e32 v36, v36, v58
	v_mul_f32_e32 v26, v26, v59
	v_mul_f32_e32 v59, v84, v78
	v_mul_f32_e32 v28, v28, v79
	v_cvt_pk_fp8_f32 v2, v36, v26
	v_cvt_pk_fp8_f32 v3, v59, v28
	v_mul_f32_e32 v58, v77, v60
	v_mul_f32_e32 v27, v27, v61
	v_mul_f32_e32 v26, v85, v80
	v_mul_f32_e32 v28, v29, v81
	v_cvt_pk_fp8_f32 v2, v58, v27 op_sel:[0,0,1]
	v_cvt_pk_fp8_f32 v3, v26, v28 op_sel:[0,0,1]
	s_waitcnt vmcnt(10)
	v_lshlrev_b32_e32 v36, 16, v18
	v_and_b32_e32 v18, 0xffff0000, v18
	v_lshlrev_b32_e32 v77, 16, v19
	global_store_dwordx2 v[82:83], v[2:3], off offset:512
	v_mov_b64_e32 v[26:27], v[208:209]
	v_mov_b64_e32 v[28:29], v[210:211]
	v_mov_b64_e32 v[58:59], v[236:237]
	v_mov_b64_e32 v[60:61], v[238:239]
	v_lshlrev_b32_e32 v78, 16, v20
	v_and_b32_e32 v20, 0xffff0000, v20
	v_mul_f32_e32 v36, v4, v36
	v_mul_f32_e32 v18, v4, v18
	v_mul_f32_e32 v77, v4, v77
	v_mul_f32_e32 v78, v4, v78
	v_mul_f32_e32 v20, v4, v20
	v_mov_b32_e32 v2, v37
	v_mov_b32_e32 v3, v37
	v_and_b32_e32 v19, 0xffff0000, v19
	v_lshlrev_b32_e32 v79, 16, v21
	v_and_b32_e32 v21, 0xffff0000, v21
	v_mul_f32_e32 v19, v4, v19
	v_mul_f32_e32 v79, v4, v79
	v_mul_f32_e32 v21, v4, v21
	v_mul_f32_e32 v26, v36, v26
	v_mul_f32_e32 v18, v18, v27
	v_mul_f32_e32 v27, v77, v28
	v_mul_f32_e32 v28, v78, v58
	v_mul_f32_e32 v20, v20, v59
	v_cvt_pk_fp8_f32 v2, v26, v18
	v_cvt_pk_fp8_f32 v3, v28, v20
	v_mul_f32_e32 v19, v19, v29
	v_mul_f32_e32 v18, v79, v60
	v_mul_f32_e32 v20, v21, v61
	v_cvt_pk_fp8_f32 v2, v27, v19 op_sel:[0,0,1]
	v_cvt_pk_fp8_f32 v3, v18, v20 op_sel:[0,0,1]
	s_waitcnt vmcnt(10)
	v_lshlrev_b32_e32 v36, 16, v10
	v_and_b32_e32 v10, 0xffff0000, v10
	v_lshlrev_b32_e32 v59, 16, v12
	global_store_dwordx2 v[82:83], v[2:3], off offset:1024
	v_mov_b64_e32 v[18:19], v[240:241]
	v_mov_b64_e32 v[20:21], v[242:243]
	v_mov_b64_e32 v[26:27], v[244:245]
	v_mov_b64_e32 v[28:29], v[246:247]
	v_and_b32_e32 v12, 0xffff0000, v12
	v_lshlrev_b32_e32 v58, 16, v11
	v_and_b32_e32 v11, 0xffff0000, v11
	v_lshlrev_b32_e32 v60, 16, v13
	v_and_b32_e32 v13, 0xffff0000, v13
	v_mul_f32_e32 v36, v4, v36
	v_mul_f32_e32 v10, v4, v10
	v_mul_f32_e32 v59, v4, v59
	v_mul_f32_e32 v12, v4, v12
	v_mov_b32_e32 v2, v37
	v_mov_b32_e32 v3, v37
	v_mul_f32_e32 v58, v4, v58
	v_mul_f32_e32 v11, v4, v11
	v_mul_f32_e32 v60, v4, v60
	v_mul_f32_e32 v4, v4, v13
	v_mul_f32_e32 v13, v36, v18
	v_mul_f32_e32 v10, v10, v19
	v_mul_f32_e32 v19, v59, v26
	v_mul_f32_e32 v12, v12, v27
	v_cvt_pk_fp8_f32 v2, v13, v10
	v_cvt_pk_fp8_f32 v3, v19, v12
	v_mul_f32_e32 v18, v58, v20
	v_mul_f32_e32 v11, v11, v21
	v_mul_f32_e32 v10, v60, v28
	v_mul_f32_e32 v4, v4, v29
	v_cvt_pk_fp8_f32 v2, v18, v11 op_sel:[0,0,1]
	v_cvt_pk_fp8_f32 v3, v10, v4 op_sel:[0,0,1]
	s_waitcnt vmcnt(6)
	v_lshlrev_b32_e32 v4, 16, v30
	v_and_b32_e32 v26, 0xffff0000, v30
	v_lshlrev_b32_e32 v27, 16, v31
	global_store_dwordx2 v[82:83], v[2:3], off offset:1536
	v_mov_b64_e32 v[10:11], v[120:121]
	v_mov_b64_e32 v[12:13], v[122:123]
	v_mov_b64_e32 v[18:19], v[124:125]
	v_mov_b64_e32 v[20:21], v[126:127]
	v_and_b32_e32 v28, 0xffff0000, v31
	v_lshlrev_b32_e32 v29, 16, v32
	v_and_b32_e32 v30, 0xffff0000, v32
	v_mul_f32_e32 v4, v5, v4
	v_mul_f32_e32 v26, v5, v26
	v_mul_f32_e32 v27, v5, v27
	v_mul_f32_e32 v28, v5, v28
	v_mul_f32_e32 v29, v5, v29
	v_mul_f32_e32 v30, v5, v30
	v_mov_b32_e32 v2, v37
	v_mov_b32_e32 v3, v37
	v_lshlrev_b32_e32 v31, 16, v33
	v_and_b32_e32 v32, 0xffff0000, v33
	v_mul_f32_e32 v31, v5, v31
	v_mul_f32_e32 v32, v5, v32
	v_mul_f32_e32 v4, v4, v10
	v_mul_f32_e32 v10, v26, v11
	v_mul_f32_e32 v11, v27, v12
	v_mul_f32_e32 v12, v28, v13
	v_mul_f32_e32 v13, v29, v18
	v_mul_f32_e32 v18, v30, v19
	v_cvt_pk_fp8_f32 v2, v4, v10
	v_cvt_pk_fp8_f32 v3, v13, v18
	v_mul_f32_e32 v4, v31, v20
	v_mul_f32_e32 v10, v32, v21
	v_cvt_pk_fp8_f32 v2, v11, v12 op_sel:[0,0,1]
	v_cvt_pk_fp8_f32 v3, v4, v10 op_sel:[0,0,1]
	v_lshl_add_u64 v[26:27], v[44:45], 0, s[2:3]
	s_waitcnt vmcnt(6)
	v_lshlrev_b32_e32 v4, 16, v22
	v_and_b32_e32 v22, 0xffff0000, v22
	global_store_dwordx2 v[26:27], v[2:3], off
	v_mov_b64_e32 v[10:11], v[200:201]
	v_mov_b64_e32 v[12:13], v[202:203]
	v_mov_b64_e32 v[18:19], v[204:205]
	v_mov_b64_e32 v[20:21], v[206:207]
	v_lshlrev_b32_e32 v28, 16, v23
	v_and_b32_e32 v23, 0xffff0000, v23
	v_lshlrev_b32_e32 v29, 16, v24
	v_and_b32_e32 v24, 0xffff0000, v24
	v_mul_f32_e32 v4, v5, v4
	v_mul_f32_e32 v22, v5, v22
	v_mul_f32_e32 v28, v5, v28
	v_mul_f32_e32 v23, v5, v23
	v_mul_f32_e32 v29, v5, v29
	v_mul_f32_e32 v24, v5, v24
	v_mov_b32_e32 v2, v37
	v_mov_b32_e32 v3, v37
	v_lshlrev_b32_e32 v30, 16, v25
	v_and_b32_e32 v25, 0xffff0000, v25
	v_mul_f32_e32 v30, v5, v30
	v_mul_f32_e32 v25, v5, v25
	v_mul_f32_e32 v4, v4, v10
	v_mul_f32_e32 v10, v22, v11
	v_mul_f32_e32 v11, v28, v12
	v_mul_f32_e32 v12, v23, v13
	v_mul_f32_e32 v13, v29, v18
	v_mul_f32_e32 v18, v24, v19
	v_cvt_pk_fp8_f32 v2, v4, v10
	v_cvt_pk_fp8_f32 v3, v13, v18
	v_mul_f32_e32 v4, v30, v20
	v_mul_f32_e32 v10, v25, v21
	v_cvt_pk_fp8_f32 v2, v11, v12 op_sel:[0,0,1]
	v_cvt_pk_fp8_f32 v3, v4, v10 op_sel:[0,0,1]
	s_waitcnt vmcnt(6)
	v_lshlrev_b32_e32 v4, 16, v14
	v_and_b32_e32 v14, 0xffff0000, v14
	v_lshlrev_b32_e32 v22, 16, v15
	global_store_dwordx2 v[26:27], v[2:3], off offset:512
	v_mov_b64_e32 v[10:11], v[208:209]
	v_mov_b64_e32 v[12:13], v[210:211]
	v_mov_b64_e32 v[18:19], v[236:237]
	v_mov_b64_e32 v[20:21], v[238:239]
	v_and_b32_e32 v15, 0xffff0000, v15
	v_lshlrev_b32_e32 v23, 16, v16
	v_and_b32_e32 v16, 0xffff0000, v16
	v_mul_f32_e32 v4, v5, v4
	v_mul_f32_e32 v14, v5, v14
	v_mul_f32_e32 v22, v5, v22
	v_mul_f32_e32 v15, v5, v15
	v_mul_f32_e32 v23, v5, v23
	v_mul_f32_e32 v16, v5, v16
	v_mov_b32_e32 v2, v37
	v_mov_b32_e32 v3, v37
	v_lshlrev_b32_e32 v24, 16, v17
	v_and_b32_e32 v17, 0xffff0000, v17
	v_mul_f32_e32 v24, v5, v24
	v_mul_f32_e32 v17, v5, v17
	v_mul_f32_e32 v4, v4, v10
	v_mul_f32_e32 v10, v14, v11
	v_mul_f32_e32 v11, v22, v12
	v_mul_f32_e32 v12, v15, v13
	v_mul_f32_e32 v13, v23, v18
	v_mul_f32_e32 v14, v16, v19
	v_cvt_pk_fp8_f32 v2, v4, v10
	v_cvt_pk_fp8_f32 v3, v13, v14
	v_mul_f32_e32 v4, v24, v20
	v_mul_f32_e32 v10, v17, v21
	v_cvt_pk_fp8_f32 v2, v11, v12 op_sel:[0,0,1]
	v_cvt_pk_fp8_f32 v3, v4, v10 op_sel:[0,0,1]
	s_waitcnt vmcnt(6)
	v_lshlrev_b32_e32 v4, 16, v6
	v_and_b32_e32 v6, 0xffff0000, v6
	v_lshlrev_b32_e32 v19, 16, v8
	global_store_dwordx2 v[26:27], v[2:3], off offset:1024
	v_mov_b64_e32 v[10:11], v[240:241]
	v_mov_b64_e32 v[12:13], v[242:243]
	v_mov_b64_e32 v[14:15], v[244:245]
	v_mov_b64_e32 v[16:17], v[246:247]
	v_and_b32_e32 v8, 0xffff0000, v8
	v_mul_f32_e32 v4, v5, v4
	v_mul_f32_e32 v6, v5, v6
	v_mul_f32_e32 v19, v5, v19
	v_mul_f32_e32 v8, v5, v8
	v_mov_b32_e32 v2, v37
	v_mov_b32_e32 v3, v37
	v_lshlrev_b32_e32 v18, 16, v7
	v_and_b32_e32 v7, 0xffff0000, v7
	v_lshlrev_b32_e32 v20, 16, v9
	v_and_b32_e32 v9, 0xffff0000, v9
	v_mul_f32_e32 v18, v5, v18
	v_mul_f32_e32 v7, v5, v7
	v_mul_f32_e32 v20, v5, v20
	v_mul_f32_e32 v5, v5, v9
	v_mul_f32_e32 v4, v4, v10
	v_mul_f32_e32 v6, v6, v11
	v_mul_f32_e32 v10, v19, v14
	v_mul_f32_e32 v8, v8, v15
	v_cvt_pk_fp8_f32 v2, v4, v6
	v_cvt_pk_fp8_f32 v3, v10, v8
	v_mul_f32_e32 v9, v18, v12
	v_mul_f32_e32 v7, v7, v13
	v_mul_f32_e32 v4, v20, v16
	v_mul_f32_e32 v5, v5, v17
	v_cvt_pk_fp8_f32 v2, v9, v7 op_sel:[0,0,1]
	v_cvt_pk_fp8_f32 v3, v4, v5 op_sel:[0,0,1]
	global_store_dwordx2 v[26:27], v[2:3], off offset:1536

.LBB0_1001:
	s_or_b64 exec, exec, s[2:3]
	s_andn2_b64 vcc, exec, s[96:97]
	s_cbranch_vccnz .LBB0_984
	s_waitcnt vmcnt(0)
	s_lshl_b32 s0, s0, 3
	s_add_i32 s12, s0, s5
	s_ashr_i32 s13, s12, 31
	s_lshl_b64 s[2:3], s[12:13], 12
	v_lshl_add_u64 v[22:23], v[40:41], 0, s[2:3]
	global_load_dwordx4 v[10:13], v[22:23], off
	v_mov_b64_e32 v[18:19], v[120:121]
	v_mov_b64_e32 v[20:21], v[122:123]
	v_mov_b64_e32 v[14:15], v[124:125]
	v_mov_b64_e32 v[16:17], v[126:127]
	s_add_i32 s0, s1, 0
	v_mov_b32_e32 v2, s0
	ds_read_b128 v[6:9], v2
	ds_read_b128 v[2:5], v2 offset:16
	v_mov_b32_e32 v24, v37
	v_mov_b32_e32 v25, v37
	s_add_i32 s14, s12, 1
	s_ashr_i32 s15, s14, 31
	s_lshl_b64 s[0:1], s[12:13], 11
	s_lshl_b64 s[2:3], s[14:15], 12
	v_lshl_add_u64 v[86:87], v[44:45], 0, s[0:1]
	global_load_dwordx4 v[26:29], v[22:23], off offset:1024
	global_load_dwordx4 v[30:33], v[22:23], off offset:2048
	global_load_dwordx4 v[58:61], v[22:23], off offset:3072
	v_lshl_add_u64 v[22:23], v[40:41], 0, s[2:3]
	v_mov_b32_e32 v88, v37
	v_mov_b32_e32 v89, v37
	s_add_i32 s2, s12, 2
	s_ashr_i32 s3, s2, 31
	s_lshl_b64 s[0:1], s[2:3], 12
	s_lshl_b64 s[14:15], s[14:15], 11
	s_lshl_b64 s[2:3], s[2:3], 11
	s_add_i32 s16, s12, 6
	s_ashr_i32 s17, s16, 31
	s_waitcnt vmcnt(3)
	v_lshlrev_b32_e32 v36, 16, v10
	v_and_b32_e32 v10, 0xffff0000, v10
	v_lshlrev_b32_e32 v78, 16, v12
	v_and_b32_e32 v12, 0xffff0000, v12
	s_waitcnt lgkmcnt(0)
	v_mul_f32_e32 v36, v6, v36
	v_mul_f32_e32 v10, v6, v10
	v_mul_f32_e32 v78, v6, v78
	v_mul_f32_e32 v12, v6, v12
	v_mul_f32_e32 v18, v36, v18
	v_mul_f32_e32 v10, v10, v19
	v_mul_f32_e32 v14, v78, v14
	v_mul_f32_e32 v12, v12, v15
	v_cvt_pk_fp8_f32 v24, v18, v10
	v_cvt_pk_fp8_f32 v25, v14, v12
	v_lshlrev_b32_e32 v77, 16, v11
	v_and_b32_e32 v11, 0xffff0000, v11
	v_lshlrev_b32_e32 v79, 16, v13
	v_and_b32_e32 v13, 0xffff0000, v13
	v_mul_f32_e32 v77, v6, v77
	v_mul_f32_e32 v11, v6, v11
	v_mul_f32_e32 v79, v6, v79
	v_mul_f32_e32 v13, v6, v13
	v_mul_f32_e32 v19, v77, v20
	v_mul_f32_e32 v11, v11, v21
	v_mul_f32_e32 v10, v79, v16
	v_mul_f32_e32 v12, v13, v17
	v_cvt_pk_fp8_f32 v24, v19, v11 op_sel:[0,0,1]
	v_cvt_pk_fp8_f32 v25, v10, v12 op_sel:[0,0,1]
	global_load_dwordx4 v[10:13], v[22:23], off
	global_load_dwordx4 v[14:17], v[22:23], off offset:1024
	global_load_dwordx4 v[18:21], v[22:23], off offset:2048
	global_load_dwordx4 v[78:81], v[22:23], off offset:3072
	s_waitcnt vmcnt(6)
	v_lshlrev_b32_e32 v36, 16, v26
	v_and_b32_e32 v26, 0xffff0000, v26
	global_store_dwordx2 v[86:87], v[24:25], off
	v_mov_b64_e32 v[22:23], v[200:201]
	v_mov_b64_e32 v[24:25], v[202:203]
	s_nop 0
	v_mov_b64_e32 v[82:83], v[204:205]
	v_mov_b64_e32 v[84:85], v[206:207]
	v_lshlrev_b32_e32 v77, 16, v27
	v_and_b32_e32 v27, 0xffff0000, v27
	v_lshlrev_b32_e32 v90, 16, v28
	v_and_b32_e32 v28, 0xffff0000, v28
	v_mul_f32_e32 v36, v6, v36
	v_mul_f32_e32 v26, v6, v26
	v_mul_f32_e32 v27, v6, v27
	v_mul_f32_e32 v90, v6, v90
	v_mul_f32_e32 v28, v6, v28
	v_lshlrev_b32_e32 v91, 16, v29
	v_and_b32_e32 v29, 0xffff0000, v29
	v_mul_f32_e32 v77, v6, v77
	v_mul_f32_e32 v91, v6, v91
	v_mul_f32_e32 v29, v6, v29
	v_mul_f32_e32 v22, v36, v22
	v_mul_f32_e32 v23, v26, v23
	v_mul_f32_e32 v25, v27, v25
	v_mul_f32_e32 v26, v90, v82
	v_mul_f32_e32 v27, v28, v83
	v_cvt_pk_fp8_f32 v88, v22, v23
	v_cvt_pk_fp8_f32 v89, v26, v27
	v_mul_f32_e32 v24, v77, v24
	v_mul_f32_e32 v22, v91, v84
	v_mul_f32_e32 v23, v29, v85
	v_cvt_pk_fp8_f32 v88, v24, v25 op_sel:[0,0,1]
	v_cvt_pk_fp8_f32 v89, v22, v23 op_sel:[0,0,1]
	s_waitcnt vmcnt(6)
	v_lshlrev_b32_e32 v36, 16, v30
	v_and_b32_e32 v30, 0xffff0000, v30
	v_lshlrev_b32_e32 v84, 16, v32
	global_store_dwordx2 v[86:87], v[88:89], off offset:512
	v_mov_b64_e32 v[22:23], v[208:209]
	v_mov_b64_e32 v[24:25], v[210:211]
	v_mov_b64_e32 v[26:27], v[236:237]
	v_mov_b64_e32 v[28:29], v[238:239]
	v_and_b32_e32 v32, 0xffff0000, v32
	v_mul_f32_e32 v36, v6, v36
	v_mul_f32_e32 v30, v6, v30
	v_mul_f32_e32 v84, v6, v84
	v_mul_f32_e32 v32, v6, v32
	v_mov_b32_e32 v82, v37
	v_mov_b32_e32 v83, v37
	v_lshlrev_b32_e32 v77, 16, v31
	v_and_b32_e32 v31, 0xffff0000, v31
	v_lshlrev_b32_e32 v85, 16, v33
	v_and_b32_e32 v33, 0xffff0000, v33
	v_mul_f32_e32 v77, v6, v77
	v_mul_f32_e32 v31, v6, v31
	v_mul_f32_e32 v85, v6, v85
	v_mul_f32_e32 v33, v6, v33
	v_mov_b32_e32 v88, v37
	v_mov_b32_e32 v89, v37
	s_waitcnt vmcnt(4)
	v_lshlrev_b32_e32 v90, 16, v17
	v_and_b32_e32 v17, 0xffff0000, v17
	v_mul_f32_e32 v90, v7, v90
	v_mul_f32_e32 v17, v7, v17
	v_mul_f32_e32 v22, v36, v22
	v_mul_f32_e32 v23, v30, v23
	v_mul_f32_e32 v26, v84, v26
	v_mul_f32_e32 v27, v32, v27
	v_cvt_pk_fp8_f32 v82, v22, v23
	v_cvt_pk_fp8_f32 v83, v26, v27
	v_mul_f32_e32 v24, v77, v24
	v_mul_f32_e32 v25, v31, v25
	v_mul_f32_e32 v22, v85, v28
	v_mul_f32_e32 v23, v33, v29
	v_cvt_pk_fp8_f32 v82, v24, v25 op_sel:[0,0,1]
	v_cvt_pk_fp8_f32 v83, v22, v23 op_sel:[0,0,1]
	v_lshlrev_b32_e32 v32, 16, v58
	v_and_b32_e32 v33, 0xffff0000, v58
	v_lshlrev_b32_e32 v36, 16, v59
	global_store_dwordx2 v[86:87], v[82:83], off offset:1024
	v_mov_b64_e32 v[22:23], v[240:241]
	v_mov_b64_e32 v[24:25], v[242:243]
	v_mov_b64_e32 v[26:27], v[244:245]
	v_mov_b64_e32 v[28:29], v[246:247]
	v_and_b32_e32 v58, 0xffff0000, v59
	v_lshlrev_b32_e32 v59, 16, v60
	v_and_b32_e32 v60, 0xffff0000, v60
	v_mul_f32_e32 v32, v6, v32
	v_mul_f32_e32 v33, v6, v33
	v_mul_f32_e32 v59, v6, v59
	v_mul_f32_e32 v60, v6, v60
	v_mov_b32_e32 v30, v37
	v_mov_b32_e32 v31, v37
	v_lshlrev_b32_e32 v77, 16, v61
	v_and_b32_e32 v61, 0xffff0000, v61
	v_mul_f32_e32 v36, v6, v36
	v_mul_f32_e32 v58, v6, v58
	v_mul_f32_e32 v77, v6, v77
	v_mul_f32_e32 v6, v6, v61
	v_mul_f32_e32 v22, v32, v22
	v_mul_f32_e32 v23, v33, v23
	v_mul_f32_e32 v26, v59, v26
	v_mul_f32_e32 v27, v60, v27
	v_cvt_pk_fp8_f32 v30, v22, v23
	v_cvt_pk_fp8_f32 v31, v26, v27
	v_mul_f32_e32 v24, v36, v24
	v_mul_f32_e32 v25, v58, v25
	v_mul_f32_e32 v22, v77, v28
	v_mul_f32_e32 v6, v6, v29
	v_cvt_pk_fp8_f32 v30, v24, v25 op_sel:[0,0,1]
	v_cvt_pk_fp8_f32 v31, v22, v6 op_sel:[0,0,1]
	v_lshlrev_b32_e32 v6, 16, v10
	v_and_b32_e32 v10, 0xffff0000, v10
	v_mul_f32_e32 v6, v7, v6
	global_store_dwordx2 v[86:87], v[30:31], off offset:1536
	v_mov_b64_e32 v[22:23], v[120:121]
	v_mov_b64_e32 v[24:25], v[122:123]
	v_mov_b64_e32 v[26:27], v[124:125]
	v_mov_b64_e32 v[28:29], v[126:127]
	v_lshlrev_b32_e32 v31, 16, v12
	v_and_b32_e32 v12, 0xffff0000, v12
	v_mul_f32_e32 v10, v7, v10
	v_mul_f32_e32 v31, v7, v31
	v_mul_f32_e32 v12, v7, v12
	v_mov_b32_e32 v58, v37
	v_mov_b32_e32 v59, v37
	v_lshlrev_b32_e32 v30, 16, v11
	v_and_b32_e32 v11, 0xffff0000, v11
	v_lshlrev_b32_e32 v32, 16, v13
	v_and_b32_e32 v13, 0xffff0000, v13
	v_mul_f32_e32 v30, v7, v30
	v_mul_f32_e32 v11, v7, v11
	v_mul_f32_e32 v32, v7, v32
	v_mul_f32_e32 v13, v7, v13
	v_lshl_add_u64 v[60:61], v[40:41], 0, s[0:1]
	v_lshl_add_u64 v[86:87], v[44:45], 0, s[14:15]
	v_lshlrev_b32_e32 v77, 16, v16
	v_and_b32_e32 v16, 0xffff0000, v16
	v_mul_f32_e32 v77, v7, v77
	v_mul_f32_e32 v16, v7, v16
	v_lshlrev_b32_e32 v36, 16, v15
	v_and_b32_e32 v15, 0xffff0000, v15
	v_mul_f32_e32 v36, v7, v36
	v_mul_f32_e32 v15, v7, v15
	s_add_i32 s14, s12, 3
	s_ashr_i32 s15, s14, 31
	s_lshl_b64 s[0:1], s[14:15], 12
	s_lshl_b64 s[14:15], s[14:15], 11
	v_mul_f32_e32 v6, v6, v22
	v_mul_f32_e32 v10, v10, v23
	v_mul_f32_e32 v23, v31, v26
	v_mul_f32_e32 v12, v12, v27
	v_cvt_pk_fp8_f32 v58, v6, v10
	v_cvt_pk_fp8_f32 v59, v23, v12
	v_mul_f32_e32 v22, v30, v24
	v_mul_f32_e32 v11, v11, v25
	v_mul_f32_e32 v6, v32, v28
	v_mul_f32_e32 v10, v13, v29
	v_cvt_pk_fp8_f32 v58, v22, v11 op_sel:[0,0,1]
	v_cvt_pk_fp8_f32 v59, v6, v10 op_sel:[0,0,1]
	global_load_dwordx4 v[10:13], v[60:61], off offset:3072
	global_load_dwordx4 v[22:25], v[60:61], off offset:2048
	global_load_dwordx4 v[26:29], v[60:61], off offset:1024
	global_load_dwordx4 v[30:33], v[60:61], off
	v_lshlrev_b32_e32 v6, 16, v14
	v_and_b32_e32 v14, 0xffff0000, v14
	global_store_dwordx2 v[86:87], v[58:59], off
	v_mov_b64_e32 v[58:59], v[200:201]
	v_mov_b64_e32 v[60:61], v[202:203]
	s_nop 0
	v_mov_b64_e32 v[82:83], v[204:205]
	v_mov_b64_e32 v[84:85], v[206:207]
	v_mul_f32_e32 v6, v7, v6
	v_mul_f32_e32 v14, v7, v14
	v_mul_f32_e32 v6, v6, v58
	v_mul_f32_e32 v14, v14, v59
	v_mul_f32_e32 v58, v77, v82
	v_mul_f32_e32 v16, v16, v83
	v_cvt_pk_fp8_f32 v88, v6, v14
	v_cvt_pk_fp8_f32 v89, v58, v16
	v_mul_f32_e32 v36, v36, v60
	v_mul_f32_e32 v15, v15, v61
	v_mul_f32_e32 v6, v90, v84
	v_mul_f32_e32 v14, v17, v85
	v_cvt_pk_fp8_f32 v88, v36, v15 op_sel:[0,0,1]
	v_cvt_pk_fp8_f32 v89, v6, v14 op_sel:[0,0,1]
	s_waitcnt vmcnt(10)
	v_lshlrev_b32_e32 v6, 16, v18
	v_and_b32_e32 v18, 0xffff0000, v18
	v_lshlrev_b32_e32 v36, 16, v19
	global_store_dwordx2 v[86:87], v[88:89], off offset:512
	v_mov_b64_e32 v[14:15], v[208:209]
	v_mov_b64_e32 v[16:17], v[210:211]
	v_mov_b64_e32 v[58:59], v[236:237]
	v_mov_b64_e32 v[60:61], v[238:239]
	v_and_b32_e32 v19, 0xffff0000, v19
	v_lshlrev_b32_e32 v77, 16, v20
	v_and_b32_e32 v20, 0xffff0000, v20
	v_mul_f32_e32 v6, v7, v6
	v_mul_f32_e32 v18, v7, v18
	v_mul_f32_e32 v36, v7, v36
	v_mul_f32_e32 v19, v7, v19
	v_mul_f32_e32 v77, v7, v77
	v_mul_f32_e32 v20, v7, v20
	v_mov_b32_e32 v82, v37
	v_mov_b32_e32 v83, v37
	v_lshlrev_b32_e32 v84, 16, v21
	v_and_b32_e32 v21, 0xffff0000, v21
	v_mul_f32_e32 v84, v7, v84
	v_mul_f32_e32 v21, v7, v21
	s_waitcnt vmcnt(3)
	v_lshlrev_b32_e32 v88, 16, v28
	v_and_b32_e32 v28, 0xffff0000, v28
	v_mul_f32_e32 v88, v8, v88
	v_mul_f32_e32 v28, v8, v28
	v_lshlrev_b32_e32 v89, 16, v29
	v_and_b32_e32 v29, 0xffff0000, v29
	v_mul_f32_e32 v89, v8, v89
	v_mul_f32_e32 v29, v8, v29
	v_mul_f32_e32 v6, v6, v14
	v_mul_f32_e32 v14, v18, v15
	v_mul_f32_e32 v15, v36, v16
	v_mul_f32_e32 v16, v19, v17
	v_mul_f32_e32 v17, v77, v58
	v_mul_f32_e32 v18, v20, v59
	v_cvt_pk_fp8_f32 v82, v6, v14
	v_cvt_pk_fp8_f32 v83, v17, v18
	v_mul_f32_e32 v6, v84, v60
	v_mul_f32_e32 v14, v21, v61
	v_cvt_pk_fp8_f32 v82, v15, v16 op_sel:[0,0,1]
	v_cvt_pk_fp8_f32 v83, v6, v14 op_sel:[0,0,1]
	v_lshlrev_b32_e32 v6, 16, v78
	v_and_b32_e32 v36, 0xffff0000, v78
	v_lshlrev_b32_e32 v60, 16, v79
	global_store_dwordx2 v[86:87], v[82:83], off offset:1024
	v_mov_b64_e32 v[14:15], v[240:241]
	v_mov_b64_e32 v[16:17], v[242:243]
	v_mov_b64_e32 v[18:19], v[244:245]
	v_mov_b64_e32 v[20:21], v[246:247]
	v_and_b32_e32 v61, 0xffff0000, v79
	v_lshlrev_b32_e32 v77, 16, v80
	v_and_b32_e32 v78, 0xffff0000, v80
	v_mul_f32_e32 v6, v7, v6
	v_mul_f32_e32 v36, v7, v36
	v_mul_f32_e32 v60, v7, v60
	v_mul_f32_e32 v61, v7, v61
	v_mul_f32_e32 v77, v7, v77
	v_mul_f32_e32 v78, v7, v78
	v_mov_b32_e32 v58, v37
	v_mov_b32_e32 v59, v37
	v_lshlrev_b32_e32 v79, 16, v81
	v_and_b32_e32 v80, 0xffff0000, v81
	v_mul_f32_e32 v79, v7, v79
	v_mul_f32_e32 v7, v7, v80
	v_lshl_add_u64 v[82:83], v[40:41], 0, s[0:1]
	v_mul_f32_e32 v6, v6, v14
	v_mul_f32_e32 v14, v36, v15
	v_mul_f32_e32 v15, v60, v16
	v_mul_f32_e32 v16, v61, v17
	v_mul_f32_e32 v17, v77, v18
	v_mul_f32_e32 v18, v78, v19
	v_cvt_pk_fp8_f32 v58, v6, v14
	v_cvt_pk_fp8_f32 v59, v17, v18
	v_mul_f32_e32 v6, v79, v20
	v_mul_f32_e32 v7, v7, v21
	v_cvt_pk_fp8_f32 v58, v15, v16 op_sel:[0,0,1]
	v_cvt_pk_fp8_f32 v59, v6, v7 op_sel:[0,0,1]
	s_waitcnt vmcnt(3)
	v_lshlrev_b32_e32 v36, 16, v30
	v_and_b32_e32 v30, 0xffff0000, v30
	v_mul_f32_e32 v36, v8, v36
	global_store_dwordx2 v[86:87], v[58:59], off offset:1536
	v_mov_b64_e32 v[14:15], v[120:121]
	v_mov_b64_e32 v[16:17], v[122:123]
	v_mov_b64_e32 v[18:19], v[124:125]
	v_mov_b64_e32 v[20:21], v[126:127]
	v_lshlrev_b32_e32 v59, 16, v32
	v_and_b32_e32 v32, 0xffff0000, v32
	v_mul_f32_e32 v30, v8, v30
	v_mul_f32_e32 v59, v8, v59
	v_mul_f32_e32 v32, v8, v32
	v_mov_b32_e32 v6, v37
	v_mov_b32_e32 v7, v37
	v_lshlrev_b32_e32 v58, 16, v31
	v_and_b32_e32 v31, 0xffff0000, v31
	v_lshlrev_b32_e32 v60, 16, v33
	v_and_b32_e32 v33, 0xffff0000, v33
	v_mul_f32_e32 v58, v8, v58
	v_mul_f32_e32 v31, v8, v31
	v_mul_f32_e32 v60, v8, v60
	v_mul_f32_e32 v33, v8, v33
	v_lshl_add_u64 v[86:87], v[44:45], 0, s[2:3]
	v_lshlrev_b32_e32 v77, 16, v27
	v_and_b32_e32 v27, 0xffff0000, v27
	v_mul_f32_e32 v27, v8, v27
	v_mul_f32_e32 v77, v8, v77
	s_add_i32 s2, s12, 4
	s_ashr_i32 s3, s2, 31
	s_lshl_b64 s[0:1], s[2:3], 12
	s_lshl_b64 s[2:3], s[2:3], 11
	v_mul_f32_e32 v14, v36, v14
	v_mul_f32_e32 v15, v30, v15
	v_mul_f32_e32 v18, v59, v18
	v_mul_f32_e32 v19, v32, v19
	v_cvt_pk_fp8_f32 v6, v14, v15
	v_cvt_pk_fp8_f32 v7, v18, v19
	v_mul_f32_e32 v16, v58, v16
	v_mul_f32_e32 v17, v31, v17
	v_mul_f32_e32 v14, v60, v20
	v_mul_f32_e32 v15, v33, v21
	v_cvt_pk_fp8_f32 v6, v16, v17 op_sel:[0,0,1]
	v_cvt_pk_fp8_f32 v7, v14, v15 op_sel:[0,0,1]
	global_load_dwordx4 v[14:17], v[82:83], off
	global_load_dwordx4 v[30:33], v[82:83], off offset:1024
	global_load_dwordx4 v[58:61], v[82:83], off offset:2048
	global_load_dwordx4 v[78:81], v[82:83], off offset:3072
	v_lshlrev_b32_e32 v36, 16, v26
	v_and_b32_e32 v26, 0xffff0000, v26
	global_store_dwordx2 v[86:87], v[6:7], off
	v_mov_b64_e32 v[18:19], v[200:201]
	v_mov_b64_e32 v[20:21], v[202:203]
	v_mov_b64_e32 v[82:83], v[204:205]
	v_mov_b64_e32 v[84:85], v[206:207]
	v_mul_f32_e32 v36, v8, v36
	v_mul_f32_e32 v26, v8, v26
	v_mov_b32_e32 v6, v37
	v_mov_b32_e32 v7, v37
	v_mul_f32_e32 v18, v36, v18
	v_mul_f32_e32 v19, v26, v19
	v_mul_f32_e32 v21, v27, v21
	v_mul_f32_e32 v26, v88, v82
	v_mul_f32_e32 v27, v28, v83
	v_cvt_pk_fp8_f32 v6, v18, v19
	v_cvt_pk_fp8_f32 v7, v26, v27
	v_mul_f32_e32 v20, v77, v20
	v_mul_f32_e32 v18, v89, v84
	v_mul_f32_e32 v19, v29, v85
	v_cvt_pk_fp8_f32 v6, v20, v21 op_sel:[0,0,1]
	v_cvt_pk_fp8_f32 v7, v18, v19 op_sel:[0,0,1]
	v_lshlrev_b32_e32 v36, 16, v22
	v_and_b32_e32 v22, 0xffff0000, v22
	v_lshlrev_b32_e32 v77, 16, v23
	global_store_dwordx2 v[86:87], v[6:7], off offset:512
	v_mov_b64_e32 v[18:19], v[208:209]
	v_mov_b64_e32 v[20:21], v[210:211]
	v_mov_b64_e32 v[26:27], v[236:237]
	v_mov_b64_e32 v[28:29], v[238:239]
	v_and_b32_e32 v23, 0xffff0000, v23
	v_lshlrev_b32_e32 v82, 16, v24
	v_and_b32_e32 v24, 0xffff0000, v24
	v_mul_f32_e32 v36, v8, v36
	v_mul_f32_e32 v22, v8, v22
	v_mul_f32_e32 v23, v8, v23
	v_mul_f32_e32 v82, v8, v82
	v_mul_f32_e32 v24, v8, v24
	v_mov_b32_e32 v6, v37
	v_mov_b32_e32 v7, v37
	v_lshlrev_b32_e32 v83, 16, v25
	v_and_b32_e32 v25, 0xffff0000, v25
	v_mul_f32_e32 v77, v8, v77
	v_mul_f32_e32 v83, v8, v83
	v_mul_f32_e32 v25, v8, v25
	s_waitcnt vmcnt(4)
	v_lshlrev_b32_e32 v88, 16, v33
	v_and_b32_e32 v33, 0xffff0000, v33
	v_mul_f32_e32 v88, v9, v88
	v_mul_f32_e32 v33, v9, v33
	v_mul_f32_e32 v18, v36, v18
	v_mul_f32_e32 v19, v22, v19
	v_mul_f32_e32 v21, v23, v21
	v_mul_f32_e32 v22, v82, v26
	v_mul_f32_e32 v23, v24, v27
	v_cvt_pk_fp8_f32 v6, v18, v19
	v_cvt_pk_fp8_f32 v7, v22, v23
	v_mul_f32_e32 v20, v77, v20
	v_mul_f32_e32 v18, v83, v28
	v_mul_f32_e32 v19, v25, v29
	v_cvt_pk_fp8_f32 v6, v20, v21 op_sel:[0,0,1]
	v_cvt_pk_fp8_f32 v7, v18, v19 op_sel:[0,0,1]
	v_lshlrev_b32_e32 v26, 16, v10
	v_and_b32_e32 v10, 0xffff0000, v10
	v_lshlrev_b32_e32 v28, 16, v12
	global_store_dwordx2 v[86:87], v[6:7], off offset:1024
	v_mov_b64_e32 v[18:19], v[240:241]
	v_mov_b64_e32 v[20:21], v[242:243]
	v_mov_b64_e32 v[22:23], v[244:245]
	v_mov_b64_e32 v[24:25], v[246:247]
	v_and_b32_e32 v12, 0xffff0000, v12
	v_lshlrev_b32_e32 v27, 16, v11
	v_and_b32_e32 v11, 0xffff0000, v11
	v_lshlrev_b32_e32 v29, 16, v13
	v_and_b32_e32 v13, 0xffff0000, v13
	v_mul_f32_e32 v26, v8, v26
	v_mul_f32_e32 v10, v8, v10
	v_mul_f32_e32 v28, v8, v28
	v_mul_f32_e32 v12, v8, v12
	v_mov_b32_e32 v6, v37
	v_mov_b32_e32 v7, v37
	v_mul_f32_e32 v27, v8, v27
	v_mul_f32_e32 v11, v8, v11
	v_mul_f32_e32 v29, v8, v29
	v_mul_f32_e32 v8, v8, v13
	v_lshlrev_b32_e32 v36, 16, v31
	v_and_b32_e32 v31, 0xffff0000, v31
	v_lshlrev_b32_e32 v77, 16, v32
	v_and_b32_e32 v32, 0xffff0000, v32
	v_mul_f32_e32 v36, v9, v36
	v_mul_f32_e32 v31, v9, v31
	v_mul_f32_e32 v77, v9, v77
	v_mul_f32_e32 v32, v9, v32
	v_mul_f32_e32 v13, v26, v18
	v_mul_f32_e32 v10, v10, v19
	v_mul_f32_e32 v19, v28, v22
	v_mul_f32_e32 v12, v12, v23
	v_cvt_pk_fp8_f32 v6, v13, v10
	v_cvt_pk_fp8_f32 v7, v19, v12
	v_mul_f32_e32 v18, v27, v20
	v_mul_f32_e32 v11, v11, v21
	v_mul_f32_e32 v10, v29, v24
	v_mul_f32_e32 v8, v8, v25
	v_cvt_pk_fp8_f32 v6, v18, v11 op_sel:[0,0,1]
	v_cvt_pk_fp8_f32 v7, v10, v8 op_sel:[0,0,1]
	v_lshlrev_b32_e32 v8, 16, v14
	v_and_b32_e32 v14, 0xffff0000, v14
	v_lshlrev_b32_e32 v24, 16, v15
	global_store_dwordx2 v[86:87], v[6:7], off offset:1536
	v_mov_b64_e32 v[10:11], v[120:121]
	v_mov_b64_e32 v[12:13], v[122:123]
	v_mov_b64_e32 v[18:19], v[124:125]
	v_mov_b64_e32 v[20:21], v[126:127]
	v_and_b32_e32 v15, 0xffff0000, v15
	v_lshlrev_b32_e32 v25, 16, v16
	v_and_b32_e32 v16, 0xffff0000, v16
	v_mul_f32_e32 v8, v9, v8
	v_mul_f32_e32 v14, v9, v14
	v_mul_f32_e32 v24, v9, v24
	v_mul_f32_e32 v15, v9, v15
	v_mul_f32_e32 v25, v9, v25
	v_mul_f32_e32 v16, v9, v16
	v_mov_b32_e32 v6, v37
	v_mov_b32_e32 v7, v37
	v_lshlrev_b32_e32 v26, 16, v17
	v_and_b32_e32 v17, 0xffff0000, v17
	v_mul_f32_e32 v26, v9, v26
	v_mul_f32_e32 v17, v9, v17
	v_lshl_add_u64 v[22:23], v[40:41], 0, s[0:1]
	v_lshl_add_u64 v[86:87], v[44:45], 0, s[14:15]
	s_add_i32 s14, s12, 5
	s_ashr_i32 s15, s14, 31
	s_lshl_b64 s[0:1], s[14:15], 12
	s_add_i32 s12, s12, 7
	s_ashr_i32 s13, s12, 31
	v_mul_f32_e32 v8, v8, v10
	v_mul_f32_e32 v10, v14, v11
	v_mul_f32_e32 v11, v24, v12
	v_mul_f32_e32 v12, v15, v13
	v_mul_f32_e32 v13, v25, v18
	v_mul_f32_e32 v14, v16, v19
	v_cvt_pk_fp8_f32 v6, v8, v10
	v_cvt_pk_fp8_f32 v7, v13, v14
	v_mul_f32_e32 v8, v26, v20
	v_mul_f32_e32 v10, v17, v21
	v_cvt_pk_fp8_f32 v6, v11, v12 op_sel:[0,0,1]
	v_cvt_pk_fp8_f32 v7, v8, v10 op_sel:[0,0,1]
	global_load_dwordx4 v[10:13], v[22:23], off offset:3072
	global_load_dwordx4 v[18:21], v[22:23], off offset:2048
	global_load_dwordx4 v[82:85], v[22:23], off offset:1024
	global_load_dwordx4 v[14:17], v[22:23], off
	v_lshlrev_b32_e32 v8, 16, v30
	v_and_b32_e32 v30, 0xffff0000, v30
	global_store_dwordx2 v[86:87], v[6:7], off
	v_mov_b64_e32 v[22:23], v[200:201]
	v_mov_b64_e32 v[24:25], v[202:203]
	v_mov_b64_e32 v[26:27], v[204:205]
	v_mov_b64_e32 v[28:29], v[206:207]
	v_mul_f32_e32 v8, v9, v8
	v_mul_f32_e32 v30, v9, v30
	v_mov_b32_e32 v6, v37
	v_mov_b32_e32 v7, v37
	v_mul_f32_e32 v8, v8, v22
	v_mul_f32_e32 v22, v30, v23
	v_mul_f32_e32 v23, v36, v24
	v_mul_f32_e32 v24, v31, v25
	v_mul_f32_e32 v25, v77, v26
	v_mul_f32_e32 v26, v32, v27
	v_cvt_pk_fp8_f32 v6, v8, v22
	v_cvt_pk_fp8_f32 v7, v25, v26
	v_mul_f32_e32 v8, v88, v28
	v_mul_f32_e32 v22, v33, v29
	v_cvt_pk_fp8_f32 v6, v23, v24 op_sel:[0,0,1]
	v_cvt_pk_fp8_f32 v7, v8, v22 op_sel:[0,0,1]
	s_waitcnt vmcnt(10)
	v_lshlrev_b32_e32 v8, 16, v58
	v_and_b32_e32 v30, 0xffff0000, v58
	v_lshlrev_b32_e32 v31, 16, v59
	global_store_dwordx2 v[86:87], v[6:7], off offset:512
	v_mov_b64_e32 v[22:23], v[208:209]
	v_mov_b64_e32 v[24:25], v[210:211]
	v_mov_b64_e32 v[26:27], v[236:237]
	v_mov_b64_e32 v[28:29], v[238:239]
	v_and_b32_e32 v32, 0xffff0000, v59
	v_lshlrev_b32_e32 v33, 16, v60
	v_and_b32_e32 v36, 0xffff0000, v60
	v_mul_f32_e32 v8, v9, v8
	v_mul_f32_e32 v30, v9, v30
	v_mul_f32_e32 v31, v9, v31
	v_mul_f32_e32 v32, v9, v32
	v_mul_f32_e32 v33, v9, v33
	v_mul_f32_e32 v36, v9, v36
	v_mov_b32_e32 v6, v37
	v_mov_b32_e32 v7, v37
	v_lshlrev_b32_e32 v58, 16, v61
	v_and_b32_e32 v59, 0xffff0000, v61
	v_mul_f32_e32 v58, v9, v58
	v_mul_f32_e32 v59, v9, v59
	s_waitcnt vmcnt(3)
	v_and_b32_e32 v77, 0xffff0000, v82
	v_mul_f32_e32 v77, v2, v77
	v_mul_f32_e32 v8, v8, v22
	v_mul_f32_e32 v22, v30, v23
	v_mul_f32_e32 v23, v31, v24
	v_mul_f32_e32 v24, v32, v25
	v_mul_f32_e32 v25, v33, v26
	v_mul_f32_e32 v26, v36, v27
	v_cvt_pk_fp8_f32 v6, v8, v22
	v_cvt_pk_fp8_f32 v7, v25, v26
	v_mul_f32_e32 v8, v58, v28
	v_mul_f32_e32 v22, v59, v29
	v_cvt_pk_fp8_f32 v6, v23, v24 op_sel:[0,0,1]
	v_cvt_pk_fp8_f32 v7, v8, v22 op_sel:[0,0,1]
	v_lshlrev_b32_e32 v8, 16, v78
	v_and_b32_e32 v30, 0xffff0000, v78
	v_lshlrev_b32_e32 v31, 16, v79
	global_store_dwordx2 v[86:87], v[6:7], off offset:1024
	v_mov_b64_e32 v[22:23], v[240:241]
	v_mov_b64_e32 v[24:25], v[242:243]
	v_mov_b64_e32 v[26:27], v[244:245]
	v_mov_b64_e32 v[28:29], v[246:247]
	v_and_b32_e32 v32, 0xffff0000, v79
	v_lshlrev_b32_e32 v33, 16, v80
	v_and_b32_e32 v36, 0xffff0000, v80
	v_mul_f32_e32 v8, v9, v8
	v_mul_f32_e32 v30, v9, v30
	v_mul_f32_e32 v31, v9, v31
	v_mul_f32_e32 v32, v9, v32
	v_mul_f32_e32 v33, v9, v33
	v_mul_f32_e32 v36, v9, v36
	v_mov_b32_e32 v6, v37
	v_mov_b32_e32 v7, v37
	v_lshlrev_b32_e32 v58, 16, v81
	v_and_b32_e32 v59, 0xffff0000, v81
	v_mul_f32_e32 v58, v9, v58
	v_mul_f32_e32 v9, v9, v59
	v_lshl_add_u64 v[78:79], v[44:45], 0, s[2:3]
	v_mov_b32_e32 v80, v37
	v_mov_b32_e32 v81, v37
	s_lshl_b64 s[2:3], s[14:15], 11
	v_mul_f32_e32 v8, v8, v22
	v_mul_f32_e32 v22, v30, v23
	v_mul_f32_e32 v23, v31, v24
	v_mul_f32_e32 v24, v32, v25
	v_mul_f32_e32 v25, v33, v26
	v_mul_f32_e32 v26, v36, v27
	v_cvt_pk_fp8_f32 v6, v8, v22
	v_cvt_pk_fp8_f32 v7, v25, v26
	v_mul_f32_e32 v8, v58, v28
	v_mul_f32_e32 v9, v9, v29
	v_cvt_pk_fp8_f32 v6, v23, v24 op_sel:[0,0,1]
	v_cvt_pk_fp8_f32 v7, v8, v9 op_sel:[0,0,1]
	s_waitcnt vmcnt(3)
	v_lshlrev_b32_e32 v26, 16, v14
	v_and_b32_e32 v14, 0xffff0000, v14
	v_lshlrev_b32_e32 v27, 16, v15
	global_store_dwordx2 v[86:87], v[6:7], off offset:1536
	v_mov_b64_e32 v[6:7], v[120:121]
	v_mov_b64_e32 v[8:9], v[122:123]
	s_nop 0
	v_mov_b64_e32 v[22:23], v[124:125]
	v_mov_b64_e32 v[24:25], v[126:127]
	v_and_b32_e32 v15, 0xffff0000, v15
	v_lshlrev_b32_e32 v28, 16, v16
	v_and_b32_e32 v16, 0xffff0000, v16
	v_mul_f32_e32 v26, v2, v26
	v_mul_f32_e32 v14, v2, v14
	v_mul_f32_e32 v15, v2, v15
	v_mul_f32_e32 v28, v2, v28
	v_mul_f32_e32 v16, v2, v16
	v_mov_b32_e32 v30, v37
	v_mov_b32_e32 v31, v37
	v_lshlrev_b32_e32 v29, 16, v17
	v_and_b32_e32 v17, 0xffff0000, v17
	v_mul_f32_e32 v27, v2, v27
	v_mul_f32_e32 v29, v2, v29
	v_mul_f32_e32 v17, v2, v17
	v_lshl_add_u64 v[32:33], v[40:41], 0, s[0:1]
	v_lshlrev_b32_e32 v36, 16, v82
	v_lshlrev_b32_e32 v86, 16, v84
	v_and_b32_e32 v84, 0xffff0000, v84
	v_mul_f32_e32 v36, v2, v36
	v_mul_f32_e32 v86, v2, v86
	v_mul_f32_e32 v84, v2, v84
	v_lshlrev_b32_e32 v82, 16, v83
	v_and_b32_e32 v83, 0xffff0000, v83
	v_lshlrev_b32_e32 v87, 16, v85
	v_and_b32_e32 v85, 0xffff0000, v85
	v_mul_f32_e32 v82, v2, v82
	v_mul_f32_e32 v83, v2, v83
	v_mul_f32_e32 v87, v2, v87
	v_mul_f32_e32 v85, v2, v85
	s_lshl_b64 s[0:1], s[16:17], 12
	v_mul_f32_e32 v6, v26, v6
	v_mul_f32_e32 v7, v14, v7
	v_mul_f32_e32 v9, v15, v9
	v_mul_f32_e32 v14, v28, v22
	v_mul_f32_e32 v15, v16, v23
	v_cvt_pk_fp8_f32 v30, v6, v7
	v_cvt_pk_fp8_f32 v31, v14, v15
	v_mul_f32_e32 v8, v27, v8
	v_mul_f32_e32 v6, v29, v24
	v_mul_f32_e32 v7, v17, v25
	v_cvt_pk_fp8_f32 v30, v8, v9 op_sel:[0,0,1]
	v_cvt_pk_fp8_f32 v31, v6, v7 op_sel:[0,0,1]
	global_load_dwordx4 v[26:29], v[32:33], off
	global_load_dwordx4 v[22:25], v[32:33], off offset:1024
	global_load_dwordx4 v[14:17], v[32:33], off offset:2048
	global_load_dwordx4 v[6:9], v[32:33], off offset:3072
	s_nop 0
	global_store_dwordx2 v[78:79], v[30:31], off
	v_mov_b64_e32 v[30:31], v[200:201]
	v_mov_b64_e32 v[32:33], v[202:203]
	s_nop 0
	v_mov_b64_e32 v[58:59], v[204:205]
	v_mov_b64_e32 v[60:61], v[206:207]
	v_mul_f32_e32 v30, v36, v30
	v_mul_f32_e32 v31, v77, v31
	v_mul_f32_e32 v36, v86, v58
	v_mul_f32_e32 v58, v84, v59
	v_cvt_pk_fp8_f32 v80, v30, v31
	v_cvt_pk_fp8_f32 v81, v36, v58
	v_mul_f32_e32 v32, v82, v32
	v_mul_f32_e32 v33, v83, v33
	v_mul_f32_e32 v30, v87, v60
	v_mul_f32_e32 v31, v85, v61
	v_cvt_pk_fp8_f32 v80, v32, v33 op_sel:[0,0,1]
	v_cvt_pk_fp8_f32 v81, v30, v31 op_sel:[0,0,1]
	v_lshlrev_b32_e32 v36, 16, v18
	v_and_b32_e32 v18, 0xffff0000, v18
	v_lshlrev_b32_e32 v77, 16, v19
	global_store_dwordx2 v[78:79], v[80:81], off offset:512
	v_mov_b64_e32 v[30:31], v[208:209]
	v_mov_b64_e32 v[32:33], v[210:211]
	v_mov_b64_e32 v[58:59], v[236:237]
	v_mov_b64_e32 v[60:61], v[238:239]
	v_lshlrev_b32_e32 v82, 16, v20
	v_and_b32_e32 v20, 0xffff0000, v20
	v_mul_f32_e32 v36, v2, v36
	v_mul_f32_e32 v18, v2, v18
	v_mul_f32_e32 v77, v2, v77
	v_mul_f32_e32 v82, v2, v82
	v_mul_f32_e32 v20, v2, v20
	v_mov_b32_e32 v80, v37
	v_mov_b32_e32 v81, v37
	v_and_b32_e32 v19, 0xffff0000, v19
	v_lshlrev_b32_e32 v83, 16, v21
	v_and_b32_e32 v21, 0xffff0000, v21
	v_mul_f32_e32 v19, v2, v19
	v_mul_f32_e32 v83, v2, v83
	v_mul_f32_e32 v21, v2, v21
	v_mov_b32_e32 v84, v37
	v_mov_b32_e32 v85, v37
	s_waitcnt vmcnt(4)
	v_lshlrev_b32_e32 v86, 16, v25
	v_and_b32_e32 v25, 0xffff0000, v25
	v_mul_f32_e32 v86, v3, v86
	v_mul_f32_e32 v25, v3, v25
	v_mul_f32_e32 v30, v36, v30
	v_mul_f32_e32 v18, v18, v31
	v_mul_f32_e32 v31, v77, v32
	v_mul_f32_e32 v32, v82, v58
	v_mul_f32_e32 v20, v20, v59
	v_cvt_pk_fp8_f32 v80, v30, v18
	v_cvt_pk_fp8_f32 v81, v32, v20
	v_mul_f32_e32 v19, v19, v33
	v_mul_f32_e32 v18, v83, v60
	v_mul_f32_e32 v20, v21, v61
	v_cvt_pk_fp8_f32 v80, v31, v19 op_sel:[0,0,1]
	v_cvt_pk_fp8_f32 v81, v18, v20 op_sel:[0,0,1]
	v_lshlrev_b32_e32 v36, 16, v10
	v_and_b32_e32 v10, 0xffff0000, v10
	v_lshlrev_b32_e32 v61, 16, v12
	global_store_dwordx2 v[78:79], v[80:81], off offset:1024
	v_mov_b64_e32 v[18:19], v[240:241]
	v_mov_b64_e32 v[20:21], v[242:243]
	v_mov_b64_e32 v[30:31], v[244:245]
	v_mov_b64_e32 v[32:33], v[246:247]
	v_and_b32_e32 v12, 0xffff0000, v12
	v_lshlrev_b32_e32 v60, 16, v11
	v_and_b32_e32 v11, 0xffff0000, v11
	v_lshlrev_b32_e32 v77, 16, v13
	v_and_b32_e32 v13, 0xffff0000, v13
	v_mul_f32_e32 v36, v2, v36
	v_mul_f32_e32 v10, v2, v10
	v_mul_f32_e32 v61, v2, v61
	v_mul_f32_e32 v12, v2, v12
	v_mov_b32_e32 v58, v37
	v_mov_b32_e32 v59, v37
	v_mul_f32_e32 v60, v2, v60
	v_mul_f32_e32 v11, v2, v11
	v_mul_f32_e32 v77, v2, v77
	v_mul_f32_e32 v2, v2, v13
	v_lshl_add_u64 v[82:83], v[44:45], 0, s[2:3]
	s_lshl_b64 s[2:3], s[16:17], 11
	v_mul_f32_e32 v13, v36, v18
	v_mul_f32_e32 v10, v10, v19
	v_mul_f32_e32 v19, v61, v30
	v_mul_f32_e32 v12, v12, v31
	v_cvt_pk_fp8_f32 v58, v13, v10
	v_cvt_pk_fp8_f32 v59, v19, v12
	v_mul_f32_e32 v18, v60, v20
	v_mul_f32_e32 v11, v11, v21
	v_mul_f32_e32 v10, v77, v32
	v_mul_f32_e32 v2, v2, v33
	v_cvt_pk_fp8_f32 v58, v18, v11 op_sel:[0,0,1]
	v_cvt_pk_fp8_f32 v59, v10, v2 op_sel:[0,0,1]
	v_lshlrev_b32_e32 v2, 16, v26
	v_and_b32_e32 v26, 0xffff0000, v26
	v_lshlrev_b32_e32 v30, 16, v27
	global_store_dwordx2 v[78:79], v[58:59], off offset:1536
	v_mov_b64_e32 v[10:11], v[120:121]
	v_mov_b64_e32 v[12:13], v[122:123]
	v_mov_b64_e32 v[18:19], v[124:125]
	v_mov_b64_e32 v[20:21], v[126:127]
	v_and_b32_e32 v27, 0xffff0000, v27
	v_lshlrev_b32_e32 v31, 16, v28
	v_and_b32_e32 v28, 0xffff0000, v28
	v_mul_f32_e32 v2, v3, v2
	v_mul_f32_e32 v26, v3, v26
	v_mul_f32_e32 v30, v3, v30
	v_mul_f32_e32 v27, v3, v27
	v_mul_f32_e32 v31, v3, v31
	v_mul_f32_e32 v28, v3, v28
	v_mov_b32_e32 v58, v37
	v_mov_b32_e32 v59, v37
	v_lshlrev_b32_e32 v32, 16, v29
	v_and_b32_e32 v29, 0xffff0000, v29
	v_mul_f32_e32 v32, v3, v32
	v_mul_f32_e32 v29, v3, v29
	v_lshl_add_u64 v[60:61], v[40:41], 0, s[0:1]
	v_lshlrev_b32_e32 v77, 16, v24
	v_and_b32_e32 v24, 0xffff0000, v24
	v_mul_f32_e32 v77, v3, v77
	v_mul_f32_e32 v24, v3, v24
	v_lshlrev_b32_e32 v36, 16, v23
	v_and_b32_e32 v23, 0xffff0000, v23
	v_mul_f32_e32 v36, v3, v36
	v_mul_f32_e32 v23, v3, v23
	s_lshl_b64 s[0:1], s[12:13], 12
	v_mul_f32_e32 v2, v2, v10
	v_mul_f32_e32 v10, v26, v11
	v_mul_f32_e32 v11, v30, v12
	v_mul_f32_e32 v12, v27, v13
	v_mul_f32_e32 v13, v31, v18
	v_mul_f32_e32 v18, v28, v19
	v_cvt_pk_fp8_f32 v58, v2, v10
	v_cvt_pk_fp8_f32 v59, v13, v18
	v_mul_f32_e32 v2, v32, v20
	v_mul_f32_e32 v10, v29, v21
	v_cvt_pk_fp8_f32 v58, v11, v12 op_sel:[0,0,1]
	v_cvt_pk_fp8_f32 v59, v2, v10 op_sel:[0,0,1]
	global_load_dwordx4 v[30:33], v[60:61], off
	global_load_dwordx4 v[26:29], v[60:61], off offset:1024
	global_load_dwordx4 v[18:21], v[60:61], off offset:2048
	global_load_dwordx4 v[10:13], v[60:61], off offset:3072
	v_lshlrev_b32_e32 v2, 16, v22
	v_and_b32_e32 v22, 0xffff0000, v22
	global_store_dwordx2 v[82:83], v[58:59], off
	v_mov_b64_e32 v[58:59], v[200:201]
	v_mov_b64_e32 v[60:61], v[202:203]
	s_nop 0
	v_mov_b64_e32 v[78:79], v[204:205]
	v_mov_b64_e32 v[80:81], v[206:207]
	v_mul_f32_e32 v2, v3, v2
	v_mul_f32_e32 v22, v3, v22
	v_mul_f32_e32 v2, v2, v58
	v_mul_f32_e32 v22, v22, v59
	v_mul_f32_e32 v58, v77, v78
	v_mul_f32_e32 v24, v24, v79
	v_cvt_pk_fp8_f32 v84, v2, v22
	v_cvt_pk_fp8_f32 v85, v58, v24
	v_mul_f32_e32 v36, v36, v60
	v_mul_f32_e32 v23, v23, v61
	v_mul_f32_e32 v2, v86, v80
	v_mul_f32_e32 v22, v25, v81
	v_cvt_pk_fp8_f32 v84, v36, v23 op_sel:[0,0,1]
	v_cvt_pk_fp8_f32 v85, v2, v22 op_sel:[0,0,1]
	s_waitcnt vmcnt(10)
	v_lshlrev_b32_e32 v2, 16, v14
	v_and_b32_e32 v14, 0xffff0000, v14
	v_lshlrev_b32_e32 v77, 16, v16
	global_store_dwordx2 v[82:83], v[84:85], off offset:512
	v_mov_b64_e32 v[22:23], v[208:209]
	v_mov_b64_e32 v[24:25], v[210:211]
	v_mov_b64_e32 v[58:59], v[236:237]
	v_mov_b64_e32 v[60:61], v[238:239]
	v_and_b32_e32 v16, 0xffff0000, v16
	v_mul_f32_e32 v2, v3, v2
	v_mul_f32_e32 v14, v3, v14
	v_mul_f32_e32 v77, v3, v77
	v_mul_f32_e32 v16, v3, v16
	v_mov_b32_e32 v78, v37
	v_mov_b32_e32 v79, v37
	v_lshlrev_b32_e32 v36, 16, v15
	v_and_b32_e32 v15, 0xffff0000, v15
	v_lshlrev_b32_e32 v80, 16, v17
	v_and_b32_e32 v17, 0xffff0000, v17
	v_mul_f32_e32 v36, v3, v36
	v_mul_f32_e32 v15, v3, v15
	v_mul_f32_e32 v80, v3, v80
	v_mul_f32_e32 v17, v3, v17
	s_waitcnt vmcnt(4)
	v_lshlrev_b32_e32 v84, 16, v28
	v_and_b32_e32 v28, 0xffff0000, v28
	v_mul_f32_e32 v84, v4, v84
	v_mul_f32_e32 v28, v4, v28
	v_lshlrev_b32_e32 v85, 16, v29
	v_and_b32_e32 v29, 0xffff0000, v29
	v_mul_f32_e32 v85, v4, v85
	v_mul_f32_e32 v29, v4, v29
	v_mul_f32_e32 v2, v2, v22
	v_mul_f32_e32 v14, v14, v23
	v_mul_f32_e32 v23, v77, v58
	v_mul_f32_e32 v16, v16, v59
	v_cvt_pk_fp8_f32 v78, v2, v14
	v_cvt_pk_fp8_f32 v79, v23, v16
	v_mul_f32_e32 v22, v36, v24
	v_mul_f32_e32 v15, v15, v25
	v_mul_f32_e32 v2, v80, v60
	v_mul_f32_e32 v14, v17, v61
	v_cvt_pk_fp8_f32 v78, v22, v15 op_sel:[0,0,1]
	v_cvt_pk_fp8_f32 v79, v2, v14 op_sel:[0,0,1]
	v_lshlrev_b32_e32 v2, 16, v6
	v_and_b32_e32 v6, 0xffff0000, v6
	v_lshlrev_b32_e32 v60, 16, v8
	global_store_dwordx2 v[82:83], v[78:79], off offset:1024
	v_mov_b64_e32 v[14:15], v[240:241]
	v_mov_b64_e32 v[16:17], v[242:243]
	v_mov_b64_e32 v[22:23], v[244:245]
	v_mov_b64_e32 v[24:25], v[246:247]
	v_and_b32_e32 v8, 0xffff0000, v8
	v_mul_f32_e32 v2, v3, v2
	v_mul_f32_e32 v6, v3, v6
	v_mul_f32_e32 v60, v3, v60
	v_mul_f32_e32 v8, v3, v8
	v_mov_b32_e32 v58, v37
	v_mov_b32_e32 v59, v37
	v_lshlrev_b32_e32 v36, 16, v7
	v_and_b32_e32 v7, 0xffff0000, v7
	v_lshlrev_b32_e32 v61, 16, v9
	v_and_b32_e32 v9, 0xffff0000, v9
	v_mul_f32_e32 v36, v3, v36
	v_mul_f32_e32 v7, v3, v7
	v_mul_f32_e32 v61, v3, v61
	v_mul_f32_e32 v3, v3, v9
	v_lshlrev_b32_e32 v77, 16, v27
	v_and_b32_e32 v27, 0xffff0000, v27
	v_mul_f32_e32 v77, v4, v77
	v_mul_f32_e32 v27, v4, v27
	v_mul_f32_e32 v2, v2, v14
	v_mul_f32_e32 v6, v6, v15
	v_mul_f32_e32 v14, v60, v22
	v_mul_f32_e32 v8, v8, v23
	v_cvt_pk_fp8_f32 v58, v2, v6
	v_cvt_pk_fp8_f32 v59, v14, v8
	v_mul_f32_e32 v9, v36, v16
	v_mul_f32_e32 v7, v7, v17
	v_mul_f32_e32 v2, v61, v24
	v_mul_f32_e32 v3, v3, v25
	v_cvt_pk_fp8_f32 v58, v9, v7 op_sel:[0,0,1]
	v_cvt_pk_fp8_f32 v59, v2, v3 op_sel:[0,0,1]
	v_lshlrev_b32_e32 v22, 16, v30
	v_and_b32_e32 v23, 0xffff0000, v30
	v_lshlrev_b32_e32 v24, 16, v31
	global_store_dwordx2 v[82:83], v[58:59], off offset:1536
	v_mov_b64_e32 v[6:7], v[120:121]
	v_mov_b64_e32 v[8:9], v[122:123]
	v_mov_b64_e32 v[14:15], v[124:125]
	v_mov_b64_e32 v[16:17], v[126:127]
	v_and_b32_e32 v25, 0xffff0000, v31
	v_lshlrev_b32_e32 v30, 16, v32
	v_and_b32_e32 v31, 0xffff0000, v32
	v_mul_f32_e32 v22, v4, v22
	v_mul_f32_e32 v23, v4, v23
	v_mul_f32_e32 v30, v4, v30
	v_mul_f32_e32 v31, v4, v31
	v_mov_b32_e32 v2, v37
	v_mov_b32_e32 v3, v37
	v_lshlrev_b32_e32 v32, 16, v33
	v_and_b32_e32 v33, 0xffff0000, v33
	v_mul_f32_e32 v24, v4, v24
	v_mul_f32_e32 v25, v4, v25
	v_mul_f32_e32 v32, v4, v32
	v_mul_f32_e32 v33, v4, v33
	v_lshl_add_u64 v[58:59], v[40:41], 0, s[0:1]
	v_lshl_add_u64 v[82:83], v[44:45], 0, s[2:3]
	v_lshlrev_b32_e32 v36, 16, v26
	v_and_b32_e32 v26, 0xffff0000, v26
	v_mul_f32_e32 v36, v4, v36
	v_mul_f32_e32 v26, v4, v26
	s_lshl_b64 s[0:1], s[12:13], 11
	v_mul_f32_e32 v6, v22, v6
	v_mul_f32_e32 v7, v23, v7
	v_mul_f32_e32 v14, v30, v14
	v_mul_f32_e32 v15, v31, v15
	v_cvt_pk_fp8_f32 v2, v6, v7
	v_cvt_pk_fp8_f32 v3, v14, v15
	v_mul_f32_e32 v8, v24, v8
	v_mul_f32_e32 v9, v25, v9
	v_mul_f32_e32 v6, v32, v16
	v_mul_f32_e32 v7, v33, v17
	v_cvt_pk_fp8_f32 v2, v8, v9 op_sel:[0,0,1]
	v_cvt_pk_fp8_f32 v3, v6, v7 op_sel:[0,0,1]
	global_load_dwordx4 v[30:33], v[58:59], off
	global_load_dwordx4 v[22:25], v[58:59], off offset:1024
	global_load_dwordx4 v[14:17], v[58:59], off offset:2048
	global_load_dwordx4 v[6:9], v[58:59], off offset:3072
	s_nop 0
	global_store_dwordx2 v[82:83], v[2:3], off
	v_mov_b64_e32 v[58:59], v[200:201]
	v_mov_b64_e32 v[60:61], v[202:203]
	v_mov_b64_e32 v[78:79], v[204:205]
	v_mov_b64_e32 v[80:81], v[206:207]
	v_mov_b32_e32 v2, v37
	v_mov_b32_e32 v3, v37
	v_mul_f32_e32 v36, v36, v58
	v_mul_f32_e32 v26, v26, v59
	v_mul_f32_e32 v59, v84, v78
	v_mul_f32_e32 v28, v28, v79
	v_cvt_pk_fp8_f32 v2, v36, v26
	v_cvt_pk_fp8_f32 v3, v59, v28
	v_mul_f32_e32 v58, v77, v60
	v_mul_f32_e32 v27, v27, v61
	v_mul_f32_e32 v26, v85, v80
	v_mul_f32_e32 v28, v29, v81
	v_cvt_pk_fp8_f32 v2, v58, v27 op_sel:[0,0,1]
	v_cvt_pk_fp8_f32 v3, v26, v28 op_sel:[0,0,1]
	s_waitcnt vmcnt(10)
	v_lshlrev_b32_e32 v36, 16, v18
	v_and_b32_e32 v18, 0xffff0000, v18
	v_lshlrev_b32_e32 v77, 16, v19
	global_store_dwordx2 v[82:83], v[2:3], off offset:512
	v_mov_b64_e32 v[26:27], v[208:209]
	v_mov_b64_e32 v[28:29], v[210:211]
	v_mov_b64_e32 v[58:59], v[236:237]
	v_mov_b64_e32 v[60:61], v[238:239]
	v_lshlrev_b32_e32 v78, 16, v20
	v_and_b32_e32 v20, 0xffff0000, v20
	v_mul_f32_e32 v36, v4, v36
	v_mul_f32_e32 v18, v4, v18
	v_mul_f32_e32 v77, v4, v77
	v_mul_f32_e32 v78, v4, v78
	v_mul_f32_e32 v20, v4, v20
	v_mov_b32_e32 v2, v37
	v_mov_b32_e32 v3, v37
	v_and_b32_e32 v19, 0xffff0000, v19
	v_lshlrev_b32_e32 v79, 16, v21
	v_and_b32_e32 v21, 0xffff0000, v21
	v_mul_f32_e32 v19, v4, v19
	v_mul_f32_e32 v79, v4, v79
	v_mul_f32_e32 v21, v4, v21
	v_mul_f32_e32 v26, v36, v26
	v_mul_f32_e32 v18, v18, v27
	v_mul_f32_e32 v27, v77, v28
	v_mul_f32_e32 v28, v78, v58
	v_mul_f32_e32 v20, v20, v59
	v_cvt_pk_fp8_f32 v2, v26, v18
	v_cvt_pk_fp8_f32 v3, v28, v20
	v_mul_f32_e32 v19, v19, v29
	v_mul_f32_e32 v18, v79, v60
	v_mul_f32_e32 v20, v21, v61
	v_cvt_pk_fp8_f32 v2, v27, v19 op_sel:[0,0,1]
	v_cvt_pk_fp8_f32 v3, v18, v20 op_sel:[0,0,1]
	s_waitcnt vmcnt(10)
	v_lshlrev_b32_e32 v36, 16, v10
	v_and_b32_e32 v10, 0xffff0000, v10
	v_lshlrev_b32_e32 v59, 16, v12
	global_store_dwordx2 v[82:83], v[2:3], off offset:1024
	v_mov_b64_e32 v[18:19], v[240:241]
	v_mov_b64_e32 v[20:21], v[242:243]
	v_mov_b64_e32 v[26:27], v[244:245]
	v_mov_b64_e32 v[28:29], v[246:247]
	v_and_b32_e32 v12, 0xffff0000, v12
	v_lshlrev_b32_e32 v58, 16, v11
	v_and_b32_e32 v11, 0xffff0000, v11
	v_lshlrev_b32_e32 v60, 16, v13
	v_and_b32_e32 v13, 0xffff0000, v13
	v_mul_f32_e32 v36, v4, v36
	v_mul_f32_e32 v10, v4, v10
	v_mul_f32_e32 v59, v4, v59
	v_mul_f32_e32 v12, v4, v12
	v_mov_b32_e32 v2, v37
	v_mov_b32_e32 v3, v37
	v_mul_f32_e32 v58, v4, v58
	v_mul_f32_e32 v11, v4, v11
	v_mul_f32_e32 v60, v4, v60
	v_mul_f32_e32 v4, v4, v13
	v_mul_f32_e32 v13, v36, v18
	v_mul_f32_e32 v10, v10, v19
	v_mul_f32_e32 v19, v59, v26
	v_mul_f32_e32 v12, v12, v27
	v_cvt_pk_fp8_f32 v2, v13, v10
	v_cvt_pk_fp8_f32 v3, v19, v12
	v_mul_f32_e32 v18, v58, v20
	v_mul_f32_e32 v11, v11, v21
	v_mul_f32_e32 v10, v60, v28
	v_mul_f32_e32 v4, v4, v29
	v_cvt_pk_fp8_f32 v2, v18, v11 op_sel:[0,0,1]
	v_cvt_pk_fp8_f32 v3, v10, v4 op_sel:[0,0,1]
	s_waitcnt vmcnt(6)
	v_lshlrev_b32_e32 v4, 16, v30
	v_and_b32_e32 v26, 0xffff0000, v30
	v_lshlrev_b32_e32 v27, 16, v31
	global_store_dwordx2 v[82:83], v[2:3], off offset:1536
	v_mov_b64_e32 v[10:11], v[120:121]
	v_mov_b64_e32 v[12:13], v[122:123]
	v_mov_b64_e32 v[18:19], v[124:125]
	v_mov_b64_e32 v[20:21], v[126:127]
	v_and_b32_e32 v28, 0xffff0000, v31
	v_lshlrev_b32_e32 v29, 16, v32
	v_and_b32_e32 v30, 0xffff0000, v32
	v_mul_f32_e32 v4, v5, v4
	v_mul_f32_e32 v26, v5, v26
	v_mul_f32_e32 v27, v5, v27
	v_mul_f32_e32 v28, v5, v28
	v_mul_f32_e32 v29, v5, v29
	v_mul_f32_e32 v30, v5, v30
	v_mov_b32_e32 v2, v37
	v_mov_b32_e32 v3, v37
	v_lshlrev_b32_e32 v31, 16, v33
	v_and_b32_e32 v32, 0xffff0000, v33
	v_mul_f32_e32 v31, v5, v31
	v_mul_f32_e32 v32, v5, v32
	v_mul_f32_e32 v4, v4, v10
	v_mul_f32_e32 v10, v26, v11
	v_mul_f32_e32 v11, v27, v12
	v_mul_f32_e32 v12, v28, v13
	v_mul_f32_e32 v13, v29, v18
	v_mul_f32_e32 v18, v30, v19
	v_cvt_pk_fp8_f32 v2, v4, v10
	v_cvt_pk_fp8_f32 v3, v13, v18
	v_mul_f32_e32 v4, v31, v20
	v_mul_f32_e32 v10, v32, v21
	v_cvt_pk_fp8_f32 v2, v11, v12 op_sel:[0,0,1]
	v_cvt_pk_fp8_f32 v3, v4, v10 op_sel:[0,0,1]
	v_lshl_add_u64 v[26:27], v[44:45], 0, s[0:1]
	s_waitcnt vmcnt(6)
	v_lshlrev_b32_e32 v4, 16, v22
	v_and_b32_e32 v22, 0xffff0000, v22
	global_store_dwordx2 v[26:27], v[2:3], off
	v_mov_b64_e32 v[10:11], v[200:201]
	v_mov_b64_e32 v[12:13], v[202:203]
	v_mov_b64_e32 v[18:19], v[204:205]
	v_mov_b64_e32 v[20:21], v[206:207]
	v_lshlrev_b32_e32 v28, 16, v23
	v_and_b32_e32 v23, 0xffff0000, v23
	v_lshlrev_b32_e32 v29, 16, v24
	v_and_b32_e32 v24, 0xffff0000, v24
	v_mul_f32_e32 v4, v5, v4
	v_mul_f32_e32 v22, v5, v22
	v_mul_f32_e32 v28, v5, v28
	v_mul_f32_e32 v23, v5, v23
	v_mul_f32_e32 v29, v5, v29
	v_mul_f32_e32 v24, v5, v24
	v_mov_b32_e32 v2, v37
	v_mov_b32_e32 v3, v37
	v_lshlrev_b32_e32 v30, 16, v25
	v_and_b32_e32 v25, 0xffff0000, v25
	v_mul_f32_e32 v30, v5, v30
	v_mul_f32_e32 v25, v5, v25
	v_mul_f32_e32 v4, v4, v10
	v_mul_f32_e32 v10, v22, v11
	v_mul_f32_e32 v11, v28, v12
	v_mul_f32_e32 v12, v23, v13
	v_mul_f32_e32 v13, v29, v18
	v_mul_f32_e32 v18, v24, v19
	v_cvt_pk_fp8_f32 v2, v4, v10
	v_cvt_pk_fp8_f32 v3, v13, v18
	v_mul_f32_e32 v4, v30, v20
	v_mul_f32_e32 v10, v25, v21
	v_cvt_pk_fp8_f32 v2, v11, v12 op_sel:[0,0,1]
	v_cvt_pk_fp8_f32 v3, v4, v10 op_sel:[0,0,1]
	s_waitcnt vmcnt(6)
	v_lshlrev_b32_e32 v4, 16, v14
	v_and_b32_e32 v14, 0xffff0000, v14
	v_lshlrev_b32_e32 v22, 16, v15
	global_store_dwordx2 v[26:27], v[2:3], off offset:512
	v_mov_b64_e32 v[10:11], v[208:209]
	v_mov_b64_e32 v[12:13], v[210:211]
	v_mov_b64_e32 v[18:19], v[236:237]
	v_mov_b64_e32 v[20:21], v[238:239]
	v_and_b32_e32 v15, 0xffff0000, v15
	v_lshlrev_b32_e32 v23, 16, v16
	v_and_b32_e32 v16, 0xffff0000, v16
	v_mul_f32_e32 v4, v5, v4
	v_mul_f32_e32 v14, v5, v14
	v_mul_f32_e32 v22, v5, v22
	v_mul_f32_e32 v15, v5, v15
	v_mul_f32_e32 v23, v5, v23
	v_mul_f32_e32 v16, v5, v16
	v_mov_b32_e32 v2, v37
	v_mov_b32_e32 v3, v37
	v_lshlrev_b32_e32 v24, 16, v17
	v_and_b32_e32 v17, 0xffff0000, v17
	v_mul_f32_e32 v24, v5, v24
	v_mul_f32_e32 v17, v5, v17
	v_mul_f32_e32 v4, v4, v10
	v_mul_f32_e32 v10, v14, v11
	v_mul_f32_e32 v11, v22, v12
	v_mul_f32_e32 v12, v15, v13
	v_mul_f32_e32 v13, v23, v18
	v_mul_f32_e32 v14, v16, v19
	v_cvt_pk_fp8_f32 v2, v4, v10
	v_cvt_pk_fp8_f32 v3, v13, v14
	v_mul_f32_e32 v4, v24, v20
	v_mul_f32_e32 v10, v17, v21
	v_cvt_pk_fp8_f32 v2, v11, v12 op_sel:[0,0,1]
	v_cvt_pk_fp8_f32 v3, v4, v10 op_sel:[0,0,1]
	s_waitcnt vmcnt(6)
	v_lshlrev_b32_e32 v4, 16, v6
	v_and_b32_e32 v6, 0xffff0000, v6
	v_lshlrev_b32_e32 v19, 16, v8
	global_store_dwordx2 v[26:27], v[2:3], off offset:1024
	v_mov_b64_e32 v[10:11], v[240:241]
	v_mov_b64_e32 v[12:13], v[242:243]
	v_mov_b64_e32 v[14:15], v[244:245]
	v_mov_b64_e32 v[16:17], v[246:247]
	v_and_b32_e32 v8, 0xffff0000, v8
	v_mul_f32_e32 v4, v5, v4
	v_mul_f32_e32 v6, v5, v6
	v_mul_f32_e32 v19, v5, v19
	v_mul_f32_e32 v8, v5, v8
	v_mov_b32_e32 v2, v37
	v_mov_b32_e32 v3, v37
	v_lshlrev_b32_e32 v18, 16, v7
	v_and_b32_e32 v7, 0xffff0000, v7
	v_lshlrev_b32_e32 v20, 16, v9
	v_and_b32_e32 v9, 0xffff0000, v9
	v_mul_f32_e32 v18, v5, v18
	v_mul_f32_e32 v7, v5, v7
	v_mul_f32_e32 v20, v5, v20
	v_mul_f32_e32 v5, v5, v9
	v_mul_f32_e32 v4, v4, v10
	v_mul_f32_e32 v6, v6, v11
	v_mul_f32_e32 v10, v19, v14
	v_mul_f32_e32 v8, v8, v15
	v_cvt_pk_fp8_f32 v2, v4, v6
	v_cvt_pk_fp8_f32 v3, v10, v8
	v_mul_f32_e32 v9, v18, v12
	v_mul_f32_e32 v7, v7, v13
	v_mul_f32_e32 v4, v20, v16
	v_mul_f32_e32 v5, v5, v17
	v_cvt_pk_fp8_f32 v2, v9, v7 op_sel:[0,0,1]
	v_cvt_pk_fp8_f32 v3, v4, v5 op_sel:[0,0,1]
	global_store_dwordx2 v[26:27], v[2:3], off offset:1536
	s_branch .LBB0_984
